# v6 + MoE-up K-loop de-waterfall + PLE bf16 epilogue loads one batch early + LRU conv ladder keeps stores in flight + attention QK fragment reads 4 ahead
# baseline (speedup 1.0000x reference)
; #define LAS __attribute__((address_space(3)))
; __device__ __forceinline__ void attn_phase(LAS unsigned char* lds, const bf16* U, bf16* YA, const float* sinks, const float* rel_bias, int G, int c, int wbase, int y8) {
;     ...
;         const int kvh = L & 3, n = (L >> 2) & 31, b = L >> 7;
;         const int tok0 = b * SEQ + (n - 1) * 128;
;         if (kvh != kvh_tab) { kvh_tab = kvh;
;             for (int e = tid; e < 4 * 192; e += 512) { const int gg = e / 192, jj = e % 192, dist = 159 - jj;
;                 rbt[e] = (dist >= 0 && dist < 128) ? rel_bias[t5_bucket(dist) * 16 + kvh * 4 + gg] * LOG2E : -1.0e30f; } }
; #pragma unroll
;         for (int kg = 0; kg < 4; ++kg) { const int key = 64 * kg + lane; int t = tok0 + key; if (t < b * SEQ) t = b * SEQ;
;             __builtin_amdgcn_global_load_lds((const unsigned*)(U + (size_t)t * NIN + C_K + kvh * 64 + 8 * wid), (LAS unsigned*)(lds + KIMG + wid * 4096 + kg * 1024), 16, 0, 0); }
; #pragma unroll
;         for (int j = 0; j < 4; ++j) { const int kg16 = 4 * (wid & 3) + j, key = 16 * kg16 + (lane >> 2); int t = tok0 + key; if (t < b * SEQ) t = b * SEQ;
;             __builtin_amdgcn_global_load_lds((const unsigned*)(U + (size_t)t * NIN + C_V + kvh * 64 + 32 * (wid >> 2) + 8 * (lane & 3)), (LAS unsigned*)(lds + VIMG + (wid >> 2) * 16384 + kg16 * 1024), 16, 0, 0); }
;         const size_t mq0 = (size_t)b * SEQ + n * 128 + 64 * qh;
;         bf16x8 qf[2][4];
; #pragma unroll
;         for (int qt = 0; qt < 2; ++qt)
; #pragma unroll
;             for (int d0 = 0; d0 < 4; ++d0) qf[qt][d0] = *(const bf16x8*)(U + (mq0 + 32 * qt + r32) * NIN + (kvh * 4 + g) * 64 + 16 * d0 + 8 * hi);
;         asm volatile("s_waitcnt vmcnt(0)" ::: "memory"); __syncthreads();
;         const float sink2 = sinks[kvh * 4 + g] * LOG2E; const LAS float* bt = rbt + g * 192 + 31 - r32 + 4 * hi;
; #pragma unroll
;         for (int qt = 0; qt < 2; ++qt) {
;             const int iq0 = 64 * qh + 32 * qt, kt0 = iq0 >> 5; const size_t mq = mq0 + 32 * qt;
;             f32x16 p[5];
; #pragma unroll
;             for (int jt = 0; jt < 5; ++jt) { f32x16 a = {};
; #pragma unroll
;                 for (int d0 = 0; d0 < 4; ++d0) { const bf16x8 kf = *(const LAS bf16x8*)(lds + KIMG + (2 * d0 + hi) * 4096 + (32 * (kt0 + jt) + r32) * 16); a = __builtin_amdgcn_mfma_f32_32x32x16_bf16(kf, qf[qt][d0], a, 0, 0, 0); }
;                 p[jt] = a; }
.LBB0_554:
	s_or_b64 exec, exec, s[4:5]
	s_bfe_u32 s31, s33, 0x50002
	s_ashr_i32 s4, s33, 7
	s_lshl_b32 s5, s4, 12
	s_lshl_b32 s8, s31, 7
	s_or_b32 s6, s5, s8
	s_add_i32 s9, s6, 0xffffff80
	v_or_b32_e32 v4, s9, v113
	v_max_i32_e32 v2, s5, v4
	v_mov_b64_e32 v[0:1], s[10:11]
	v_mad_i64_i32 v[2:3], s[6:7], v2, s87, v[0:1]
	s_lshl_b32 s6, s84, 7
	s_mov_b32 s7, s40
	v_lshl_add_u64 v[2:3], v[2:3], 0, s[6:7]
	v_lshl_add_u64 v[2:3], v[2:3], 0, s[24:25]
	s_mov_b64 s[34:35], 0x800
	v_lshl_add_u64 v[2:3], v[2:3], 0, s[34:35]
	s_mov_b32 m0, s42
	v_mov_b32_e32 v8, 0x2c00
	global_load_lds_dwordx4 v[2:3], off
	v_or_b32_e32 v2, 64, v4
	v_max_i32_e32 v2, s5, v2
	v_mad_i64_i32 v[2:3], s[28:29], v2, s87, v[0:1]
	v_lshl_add_u64 v[2:3], v[2:3], 0, s[6:7]
	v_lshl_add_u64 v[2:3], v[2:3], 0, s[24:25]
	v_lshl_add_u64 v[2:3], v[2:3], 0, s[34:35]
	s_add_i32 m0, s42, 0x400
	v_add_u32_e32 v155, s77, v123
	global_load_lds_dwordx4 v[2:3], off
	v_add_u32_e32 v2, 0x80, v4
	v_max_i32_e32 v2, s5, v2
	v_mad_i64_i32 v[2:3], s[28:29], v2, s87, v[0:1]
	v_lshl_add_u64 v[2:3], v[2:3], 0, s[6:7]
	v_lshl_add_u64 v[2:3], v[2:3], 0, s[24:25]
	v_lshl_add_u64 v[2:3], v[2:3], 0, s[34:35]
	s_add_i32 m0, s42, 0x800
	v_add_u32_e32 v152, s59, v123
	global_load_lds_dwordx4 v[2:3], off
	v_add_u32_e32 v2, 0xc0, v4
	v_max_i32_e32 v2, s5, v2
	v_mad_i64_i32 v[2:3], s[28:29], v2, s87, v[0:1]
	v_lshl_add_u64 v[2:3], v[2:3], 0, s[6:7]
	v_lshl_add_u64 v[2:3], v[2:3], 0, s[24:25]
	v_lshl_add_u64 v[2:3], v[2:3], 0, s[34:35]
	s_add_i32 m0, s42, 0xc00
	v_or_b32_e32 v4, s9, v119
	global_load_lds_dwordx4 v[2:3], off
	v_add_u32_e32 v2, s44, v4
	v_max_i32_e32 v2, s5, v2
	v_mad_i64_i32 v[2:3], s[28:29], v2, s87, v[0:1]
	v_lshl_add_u64 v[2:3], v[2:3], 0, s[6:7]
	v_lshl_add_u64 v[2:3], v[2:3], 0, s[26:27]
	v_lshl_add_u64 v[2:3], v[2:3], 0, v[232:233]
	s_mov_b64 s[34:35], 0xa00
	v_lshl_add_u64 v[2:3], v[2:3], 0, s[34:35]
	s_mov_b32 m0, s85
	v_add_u32_e32 v153, s65, v123
	global_load_lds_dwordx4 v[2:3], off
	v_add_u32_e32 v2, s45, v4
	v_max_i32_e32 v2, s5, v2
	v_mad_i64_i32 v[2:3], s[28:29], v2, s87, v[0:1]
	v_lshl_add_u64 v[2:3], v[2:3], 0, s[6:7]
	v_lshl_add_u64 v[2:3], v[2:3], 0, s[26:27]
	v_lshl_add_u64 v[2:3], v[2:3], 0, v[232:233]
	v_lshl_add_u64 v[2:3], v[2:3], 0, s[34:35]
	s_mov_b32 m0, s48
	v_add_u32_e32 v154, s76, v123
	global_load_lds_dwordx4 v[2:3], off
	v_add_u32_e32 v2, s52, v4
	v_max_i32_e32 v2, s5, v2
	v_mad_i64_i32 v[2:3], s[28:29], v2, s87, v[0:1]
	v_lshl_add_u64 v[2:3], v[2:3], 0, s[6:7]
	v_lshl_add_u64 v[2:3], v[2:3], 0, s[26:27]
	v_lshl_add_u64 v[2:3], v[2:3], 0, v[232:233]
	v_lshl_add_u64 v[2:3], v[2:3], 0, s[34:35]
	s_mov_b32 m0, s46
	s_nop 0
	global_load_lds_dwordx4 v[2:3], off
	v_add_u32_e32 v2, s53, v4
	v_max_i32_e32 v2, s5, v2
	s_ashr_i32 s5, s4, 31
	v_mad_i64_i32 v[0:1], s[28:29], v2, s87, v[0:1]
	s_lshl_b64 s[4:5], s[4:5], 12
	v_lshl_add_u64 v[0:1], v[0:1], 0, s[6:7]
	s_or_b32 s4, s4, s8
	v_lshl_add_u64 v[0:1], v[0:1], 0, s[26:27]
	s_or_b64 s[28:29], s[4:5], s[16:17]
	s_lshl_b32 s4, s84, 8
	v_lshl_add_u64 v[0:1], v[0:1], 0, v[232:233]
	s_add_i32 s6, s4, s43
	v_lshl_add_u64 v[0:1], v[0:1], 0, s[34:35]
	s_mov_b32 m0, s47
	s_ashr_i32 s7, s6, 31
	global_load_lds_dwordx4 v[0:1], off
	v_lshl_add_u64 v[4:5], s[6:7], 1, v[110:111]
	v_or_b32_e32 v0, s28, v108
	v_mad_u64_u32 v[6:7], s[6:7], v0, s87, v[4:5]
	v_mad_i32_i24 v7, s5, v8, v7
	global_load_dwordx4 v[0:3], v[6:7], off
	global_load_dwordx4 v[96:99], v[6:7], off offset:32
	global_load_dwordx4 v[100:103], v[6:7], off offset:64
	global_load_dwordx4 v[104:107], v[6:7], off offset:96
	v_or_b32_e32 v6, s28, v118
	s_add_i32 s8, s30, s41
	v_mad_u64_u32 v[4:5], s[6:7], v6, s87, v[4:5]
	s_ashr_i32 s9, s8, 31
	v_mad_i32_i24 v5, s5, v8, v5
	s_lshl_b64 s[4:5], s[8:9], 2
	s_add_u32 s4, s36, s4
	s_addc_u32 s5, s37, s5
	global_load_dwordx4 v[92:95], v[4:5], off
	global_load_dwordx4 v[88:91], v[4:5], off offset:32
	global_load_dwordx4 v[84:87], v[4:5], off offset:64
	global_load_dwordx4 v[80:83], v[4:5], off offset:96
	s_waitcnt vmcnt(0)
	s_waitcnt vmcnt(0) lgkmcnt(0)
	s_barrier
	global_load_dword v4, v233, s[4:5]
	v_add_u32_e32 v8, s58, v123
	s_cmp_eq_u32 s31, 0
	s_cselect_b64 s[4:5], -1, 0
	s_and_b64 s[6:7], s[4:5], s[20:21]
	ds_read_b128 v[156:159], v155 offset:8192
	s_waitcnt vmcnt(0)
	v_mul_f32_e32 v151, 0x3fb8aa3b, v4
	ds_read_b128 v[180:183], v8
	ds_read_b128 v[184:187], v8 offset:8192
	ds_read_b128 v[188:191], v8 offset:16384
	ds_read_b128 v[192:195], v8 offset:24576
	s_waitcnt lgkmcnt(3)
	v_mfma_f32_32x32x16_bf16 v[64:79], v[180:183], v[0:3], 0
	ds_read_b128 v[180:183], v152
	s_waitcnt lgkmcnt(3)
	v_mfma_f32_32x32x16_bf16 v[64:79], v[184:187], v[96:99], v[64:79]
	ds_read_b128 v[184:187], v152 offset:8192
	s_waitcnt lgkmcnt(3)
	v_mfma_f32_32x32x16_bf16 v[64:79], v[188:191], v[100:103], v[64:79]
	ds_read_b128 v[188:191], v152 offset:16384
	s_waitcnt lgkmcnt(3)
	v_mfma_f32_32x32x16_bf16 v[64:79], v[192:195], v[104:107], v[64:79]
	ds_read_b128 v[192:195], v152 offset:24576
	s_waitcnt lgkmcnt(3)
	v_mfma_f32_32x32x16_bf16 v[48:63], v[180:183], v[0:3], 0
	ds_read_b128 v[180:183], v153
	s_waitcnt lgkmcnt(3)
	v_mfma_f32_32x32x16_bf16 v[48:63], v[184:187], v[96:99], v[48:63]
	ds_read_b128 v[184:187], v153 offset:8192
	s_waitcnt lgkmcnt(3)
	v_mfma_f32_32x32x16_bf16 v[48:63], v[188:191], v[100:103], v[48:63]
	ds_read_b128 v[188:191], v153 offset:16384
	s_waitcnt lgkmcnt(3)
	v_mfma_f32_32x32x16_bf16 v[48:63], v[192:195], v[104:107], v[48:63]
	ds_read_b128 v[192:195], v153 offset:24576
	s_waitcnt lgkmcnt(3)
	v_mfma_f32_32x32x16_bf16 v[32:47], v[180:183], v[0:3], 0
	ds_read_b128 v[180:183], v154
	s_waitcnt lgkmcnt(3)
; #define LAS __attribute__((address_space(3)))
; __device__ __forceinline__ int crow(int r, int hi) { return (r & 3) + 8 * (r >> 2) + 4 * hi; }
; __device__ __forceinline__ int crow(int r, int hi) { return (r & 3) + 8 * (r >> 2) + 4 * hi; }
; __device__ __forceinline__ void attn_phase(LAS unsigned char* lds, const bf16* U, bf16* YA, const float* sinks, const float* rel_bias, int G, int c, int wbase, int y8) {
;     ...
;             for (int jt = 0; jt < 5; ++jt) { f32x16 a = {};
; #pragma unroll
;                 for (int d0 = 0; d0 < 4; ++d0) { const bf16x8 kf = *(const LAS bf16x8*)(lds + KIMG + (2 * d0 + hi) * 4096 + (32 * (kt0 + jt) + r32) * 16); a = __builtin_amdgcn_mfma_f32_32x32x16_bf16(kf, qf[qt][d0], a, 0, 0, 0); }
;                 p[jt] = a; }
;             float mx = sink2;
; #pragma unroll
;             for (int jt = 0; jt < 5; ++jt)
; #pragma unroll
;                 for (int r = 0; r < 16; ++r) { float s = p[jt][r] + bt[32 * jt + (r & 3) + 8 * (r >> 2)];
;                     if (n == 0) { if (32 * (kt0 + jt) + crow(r, hi) < 128) s = -1.0e30f; }
;                     p[jt][r] = s; mx = fmaxf(mx, s); }
	v_mfma_f32_32x32x16_bf16 v[32:47], v[184:187], v[96:99], v[32:47]
	ds_read_b128 v[184:187], v154 offset:8192
	s_waitcnt lgkmcnt(3)
	v_mfma_f32_32x32x16_bf16 v[32:47], v[188:191], v[100:103], v[32:47]
	ds_read_b128 v[188:191], v154 offset:16384
	s_waitcnt lgkmcnt(3)
	v_mfma_f32_32x32x16_bf16 v[32:47], v[192:195], v[104:107], v[32:47]
	ds_read_b128 v[192:195], v154 offset:24576
	s_waitcnt lgkmcnt(3)
	v_mfma_f32_32x32x16_bf16 v[16:31], v[180:183], v[0:3], 0
	ds_read_b128 v[180:183], v155
	s_waitcnt lgkmcnt(3)
	v_mfma_f32_32x32x16_bf16 v[16:31], v[184:187], v[96:99], v[16:31]
	ds_read_b128 v[184:187], v155 offset:16384
	s_waitcnt lgkmcnt(3)
	v_mfma_f32_32x32x16_bf16 v[16:31], v[188:191], v[100:103], v[16:31]
	ds_read_b128 v[188:191], v155 offset:24576
	s_waitcnt lgkmcnt(3)
	v_mfma_f32_32x32x16_bf16 v[16:31], v[192:195], v[104:107], v[16:31]
	s_waitcnt lgkmcnt(2)
	v_mfma_f32_32x32x16_bf16 v[0:15], v[180:183], v[0:3], 0
	v_mfma_f32_32x32x16_bf16 v[0:15], v[156:159], v[96:99], v[0:15]
	s_waitcnt lgkmcnt(1)
	v_mfma_f32_32x32x16_bf16 v[0:15], v[184:187], v[100:103], v[0:15]
	v_mov_b32_e32 v102, 0xf149f2ca
	s_waitcnt lgkmcnt(0)
	v_mfma_f32_32x32x16_bf16 v[0:15], v[188:191], v[104:107], v[0:15]
	ds_read2_b32 v[96:97], v121 offset0:31 offset1:32
	ds_read2_b32 v[98:99], v121 offset0:33 offset1:34
	s_waitcnt lgkmcnt(1)
	v_add_f32_e32 v64, v64, v96
	v_cndmask_b32_e64 v96, v64, v102, s[4:5]
	v_add_f32_e32 v64, v65, v97
	s_waitcnt lgkmcnt(0)
	v_add_f32_e32 v65, v66, v98
	v_cndmask_b32_e64 v66, v65, v102, s[4:5]
	v_add_f32_e32 v65, v67, v99
	ds_read2_b32 v[98:99], v121 offset0:39 offset1:40
	v_cndmask_b32_e64 v64, v64, v102, s[4:5]
	v_max3_f32 v97, v151, v96, v64
	v_cndmask_b32_e64 v65, v65, v102, s[4:5]
	v_max3_f32 v97, v97, v66, v65
	s_waitcnt lgkmcnt(0)
	v_add_f32_e32 v67, v68, v98
	v_cndmask_b32_e64 v68, v67, v102, s[4:5]
	v_add_f32_e32 v67, v69, v99
	ds_read2_b32 v[98:99], v121 offset0:41 offset1:42
	v_cndmask_b32_e64 v67, v67, v102, s[4:5]
	v_max3_f32 v69, v97, v68, v67
	s_waitcnt lgkmcnt(0)
	v_add_f32_e32 v70, v70, v98
	v_cndmask_b32_e64 v97, v70, v102, s[4:5]
	v_add_f32_e32 v70, v71, v99
	ds_read2_b32 v[98:99], v121 offset0:47 offset1:48
	v_cndmask_b32_e64 v70, v70, v102, s[4:5]
	v_max3_f32 v100, v69, v97, v70
	s_waitcnt lgkmcnt(0)
	v_add_f32_e32 v69, v72, v98
	v_cndmask_b32_e64 v71, v69, v102, s[4:5]
	v_add_f32_e32 v69, v73, v99
	ds_read2_b32 v[98:99], v121 offset0:49 offset1:50
	v_cndmask_b32_e64 v69, v69, v102, s[4:5]
	v_max3_f32 v100, v100, v71, v69
	s_waitcnt lgkmcnt(0)
	v_add_f32_e32 v72, v74, v98
	v_cndmask_b32_e64 v73, v72, v102, s[4:5]
	v_add_f32_e32 v72, v75, v99
	ds_read2_b32 v[98:99], v121 offset0:55 offset1:56
	v_cndmask_b32_e64 v72, v72, v102, s[4:5]
	v_max3_f32 v100, v100, v73, v72
	s_waitcnt lgkmcnt(0)
	v_add_f32_e32 v74, v76, v98
	v_cndmask_b32_e64 v75, v74, v102, s[4:5]
	v_add_f32_e32 v74, v77, v99
	ds_read2_b32 v[76:77], v121 offset0:57 offset1:58
	v_cndmask_b32_e64 v74, v74, v102, s[4:5]
	v_max3_f32 v98, v100, v75, v74
	s_waitcnt lgkmcnt(0)
	v_add_f32_e32 v76, v78, v76
	v_cndmask_b32_e64 v78, v76, v102, s[4:5]
	v_add_f32_e32 v76, v79, v77
	v_cndmask_b32_e64 v76, v76, v102, s[4:5]
	v_max3_f32 v79, v98, v78, v76
	ds_read2_b32 v[98:99], v121 offset0:63 offset1:64
	s_waitcnt lgkmcnt(0)
	v_add_f32_e32 v48, v48, v98
	v_cndmask_b32_e64 v77, v48, v102, s[4:5]
	v_add_f32_e32 v48, v49, v99
	ds_read2_b32 v[98:99], v121 offset0:65 offset1:66
	v_cndmask_b32_e64 v48, v48, v102, s[4:5]
	v_max3_f32 v79, v79, v77, v48
	s_waitcnt lgkmcnt(0)
	v_add_f32_e32 v49, v50, v98
	v_cndmask_b32_e64 v50, v49, v102, s[4:5]
	v_add_f32_e32 v49, v51, v99
	ds_read2_b32 v[98:99], v121 offset0:71 offset1:72
	v_cndmask_b32_e64 v49, v49, v102, s[4:5]
	v_max3_f32 v79, v79, v50, v49
	s_waitcnt lgkmcnt(0)
	v_add_f32_e32 v51, v52, v98
	v_cndmask_b32_e64 v52, v51, v102, s[4:5]
	v_add_f32_e32 v51, v53, v99
	ds_read2_b32 v[98:99], v121 offset0:73 offset1:74
	v_cndmask_b32_e64 v51, v51, v102, s[4:5]
	v_max3_f32 v53, v79, v52, v51
	s_waitcnt lgkmcnt(0)
	v_add_f32_e32 v54, v54, v98
	v_cndmask_b32_e64 v79, v54, v102, s[4:5]
	v_add_f32_e32 v54, v55, v99
	ds_read2_b32 v[98:99], v121 offset0:79 offset1:80
	v_cndmask_b32_e64 v54, v54, v102, s[4:5]
	v_max3_f32 v100, v53, v79, v54
	s_waitcnt lgkmcnt(0)
	v_add_f32_e32 v53, v56, v98
	v_cndmask_b32_e64 v55, v53, v102, s[4:5]
	v_add_f32_e32 v53, v57, v99
	ds_read2_b32 v[98:99], v121 offset0:81 offset1:82
	v_cndmask_b32_e64 v53, v53, v102, s[4:5]
	v_max3_f32 v100, v100, v55, v53
	s_waitcnt lgkmcnt(0)
	v_add_f32_e32 v56, v58, v98
	v_cndmask_b32_e64 v57, v56, v102, s[4:5]
	v_add_f32_e32 v56, v59, v99
	ds_read2_b32 v[98:99], v121 offset0:87 offset1:88
	v_cndmask_b32_e64 v56, v56, v102, s[4:5]
	v_max3_f32 v100, v100, v57, v56
	s_waitcnt lgkmcnt(0)
	v_add_f32_e32 v58, v60, v98
	v_cndmask_b32_e64 v59, v58, v102, s[4:5]
	v_add_f32_e32 v58, v61, v99
	ds_read2_b32 v[60:61], v121 offset0:89 offset1:90
	v_cndmask_b32_e64 v58, v58, v102, s[4:5]
	v_max3_f32 v98, v100, v59, v58
	ds_read2_b32 v[100:101], v121 offset0:111 offset1:112
	s_waitcnt lgkmcnt(1)
	v_add_f32_e32 v60, v62, v60
	v_cndmask_b32_e64 v62, v60, v102, s[4:5]
	v_add_f32_e32 v60, v63, v61
	v_cndmask_b32_e64 v60, v60, v102, s[4:5]
	v_max3_f32 v63, v98, v62, v60
	ds_read2_b32 v[98:99], v121 offset0:95 offset1:96
	s_waitcnt lgkmcnt(0)
	v_add_f32_e32 v32, v32, v98
	v_cndmask_b32_e64 v61, v32, v102, s[6:7]
	v_add_f32_e32 v32, v33, v99
	ds_read2_b32 v[98:99], v121 offset0:97 offset1:98
	v_cndmask_b32_e64 v33, v32, v102, s[6:7]
	v_max3_f32 v32, v63, v61, v33
	s_waitcnt lgkmcnt(0)
; __device__ __forceinline__ int crow(int r, int hi) { return (r & 3) + 8 * (r >> 2) + 4 * hi; }
; __device__ __forceinline__ int crow(int r, int hi) { return (r & 3) + 8 * (r >> 2) + 4 * hi; }
; __device__ __forceinline__ void attn_phase(LAS unsigned char* lds, const bf16* U, bf16* YA, const float* sinks, const float* rel_bias, int G, int c, int wbase, int y8) {
;     ...
;             float mx = sink2;
; #pragma unroll
;             for (int jt = 0; jt < 5; ++jt)
; #pragma unroll
;                 for (int r = 0; r < 16; ++r) { float s = p[jt][r] + bt[32 * jt + (r & 3) + 8 * (r >> 2)];
;                     if (n == 0) { if (32 * (kt0 + jt) + crow(r, hi) < 128) s = -1.0e30f; }
;                     p[jt][r] = s; mx = fmaxf(mx, s); }
	v_add_f32_e32 v34, v34, v98
	v_cndmask_b32_e64 v63, v34, v102, s[6:7]
	v_add_f32_e32 v34, v35, v99
	ds_read2_b32 v[98:99], v121 offset0:103 offset1:104
	v_cndmask_b32_e64 v34, v34, v102, s[6:7]
	v_max3_f32 v32, v32, v63, v34
	s_waitcnt lgkmcnt(0)
	v_add_f32_e32 v35, v36, v98
	v_cndmask_b32_e64 v36, v35, v102, s[6:7]
	v_add_f32_e32 v35, v37, v99
	ds_read2_b32 v[98:99], v121 offset0:105 offset1:106
	v_cndmask_b32_e64 v35, v35, v102, s[6:7]
	v_max3_f32 v32, v32, v36, v35
	s_waitcnt lgkmcnt(0)
	v_add_f32_e32 v37, v38, v98
	v_cndmask_b32_e64 v98, v37, v102, s[6:7]
	v_add_f32_e32 v37, v39, v99
	v_cndmask_b32_e64 v38, v37, v102, s[6:7]
	v_add_f32_e32 v37, v40, v100
	v_cndmask_b32_e64 v39, v37, v102, s[6:7]
	v_add_f32_e32 v37, v41, v101
	ds_read2_b32 v[100:101], v121 offset0:113 offset1:114
	v_max3_f32 v32, v32, v98, v38
	v_cndmask_b32_e64 v37, v37, v102, s[6:7]
	v_max3_f32 v32, v32, v39, v37
	s_waitcnt lgkmcnt(0)
	v_add_f32_e32 v40, v42, v100
	v_cndmask_b32_e64 v41, v40, v102, s[6:7]
	v_add_f32_e32 v40, v43, v101
	ds_read2_b32 v[100:101], v121 offset0:119 offset1:120
	v_cndmask_b32_e64 v40, v40, v102, s[6:7]
	v_max3_f32 v32, v32, v41, v40
	s_waitcnt lgkmcnt(0)
	v_add_f32_e32 v42, v44, v100
	v_cndmask_b32_e64 v43, v42, v102, s[6:7]
	v_add_f32_e32 v42, v45, v101
	ds_read2_b32 v[44:45], v121 offset0:121 offset1:122
	ds_read2_b32 v[100:101], v121 offset0:127 offset1:128
	v_cndmask_b32_e64 v42, v42, v102, s[6:7]
	v_max3_f32 v32, v32, v43, v42
	s_waitcnt lgkmcnt(1)
	v_add_f32_e32 v44, v46, v44
	s_waitcnt lgkmcnt(0)
	v_add_f32_e32 v16, v16, v100
	v_cndmask_b32_e64 v46, v44, v102, s[6:7]
	v_add_f32_e32 v44, v47, v45
	v_cndmask_b32_e64 v45, v16, v102, s[6:7]
	v_add_f32_e32 v16, v17, v101
	ds_read2_b32 v[100:101], v121 offset0:129 offset1:130
	v_cndmask_b32_e64 v44, v44, v102, s[6:7]
	v_max3_f32 v32, v32, v46, v44
	v_cndmask_b32_e64 v16, v16, v102, s[6:7]
	v_max3_f32 v32, v32, v45, v16
	s_waitcnt lgkmcnt(0)
	v_add_f32_e32 v17, v18, v100
	v_cndmask_b32_e64 v18, v17, v102, s[6:7]
	v_add_f32_e32 v17, v19, v101
	ds_read2_b32 v[100:101], v121 offset0:135 offset1:136
	v_cndmask_b32_e64 v17, v17, v102, s[6:7]
	v_max3_f32 v32, v32, v18, v17
	s_waitcnt lgkmcnt(0)
	v_add_f32_e32 v19, v20, v100
	v_cndmask_b32_e64 v20, v19, v102, s[6:7]
	v_add_f32_e32 v19, v21, v101
	ds_read2_b32 v[100:101], v121 offset0:137 offset1:138
	v_cndmask_b32_e64 v19, v19, v102, s[6:7]
	v_max3_f32 v32, v32, v20, v19
	s_waitcnt lgkmcnt(0)
	v_add_f32_e32 v21, v22, v100
	v_cndmask_b32_e64 v22, v21, v102, s[6:7]
	v_add_f32_e32 v21, v23, v101
	ds_read2_b32 v[100:101], v121 offset0:143 offset1:144
	v_cndmask_b32_e64 v21, v21, v102, s[6:7]
	v_max3_f32 v32, v32, v22, v21
	s_waitcnt lgkmcnt(0)
	v_add_f32_e32 v23, v24, v100
	v_cndmask_b32_e64 v24, v23, v102, s[6:7]
	v_add_f32_e32 v23, v25, v101
	ds_read2_b32 v[100:101], v121 offset0:145 offset1:146
	v_cndmask_b32_e64 v23, v23, v102, s[6:7]
	v_max3_f32 v32, v32, v24, v23
	s_waitcnt lgkmcnt(0)
	v_add_f32_e32 v25, v26, v100
	v_cndmask_b32_e64 v26, v25, v102, s[6:7]
	v_add_f32_e32 v25, v27, v101
	ds_read2_b32 v[100:101], v121 offset0:151 offset1:152
	v_cndmask_b32_e64 v25, v25, v102, s[6:7]
	v_max3_f32 v32, v32, v26, v25
	s_waitcnt lgkmcnt(0)
	v_add_f32_e32 v27, v28, v100
	v_cndmask_b32_e64 v28, v27, v102, s[6:7]
	v_add_f32_e32 v27, v29, v101
	ds_read2_b32 v[100:101], v121 offset0:153 offset1:154
	v_cndmask_b32_e64 v27, v27, v102, s[6:7]
	v_max3_f32 v32, v32, v28, v27
	s_waitcnt lgkmcnt(0)
	v_add_f32_e32 v29, v30, v100
	v_cndmask_b32_e64 v30, v29, v102, s[6:7]
	v_add_f32_e32 v29, v31, v101
	ds_read2_b32 v[100:101], v121 offset0:159 offset1:160
	v_cndmask_b32_e64 v29, v29, v102, s[6:7]
	v_max3_f32 v32, v32, v30, v29
	s_waitcnt lgkmcnt(0)
	v_add_f32_e32 v47, v0, v100
	v_add_f32_e32 v31, v1, v101
	ds_read2_b32 v[0:1], v121 offset0:161 offset1:162
	v_max3_f32 v32, v32, v47, v31
	s_waitcnt lgkmcnt(0)
	v_add_f32_e32 v172, v2, v0
	v_add_f32_e32 v171, v3, v1
	ds_read2_b32 v[0:1], v121 offset0:167 offset1:168
	v_max3_f32 v2, v32, v172, v171
	s_waitcnt lgkmcnt(0)
	v_add_f32_e32 v174, v4, v0
	v_add_f32_e32 v173, v5, v1
	ds_read2_b32 v[0:1], v121 offset0:169 offset1:170
	v_max3_f32 v2, v2, v174, v173
	s_waitcnt lgkmcnt(0)
	v_add_f32_e32 v176, v6, v0
	v_add_f32_e32 v175, v7, v1
	ds_read2_b32 v[0:1], v121 offset0:175 offset1:176
	v_max3_f32 v2, v2, v176, v175
	s_waitcnt lgkmcnt(0)
	v_add_f32_e32 v177, v8, v0
	v_add_f32_e32 v8, v9, v1
	ds_read2_b32 v[0:1], v121 offset0:177 offset1:178
	v_max3_f32 v2, v2, v177, v8
	s_waitcnt lgkmcnt(0)
	v_add_f32_e32 v10, v10, v0
	v_add_f32_e32 v9, v11, v1
	ds_read2_b32 v[0:1], v121 offset0:183 offset1:184
	v_max3_f32 v2, v2, v10, v9
	s_waitcnt lgkmcnt(0)
	v_add_f32_e32 v12, v12, v0
	v_add_f32_e32 v11, v13, v1
	ds_read2_b32 v[0:1], v121 offset0:185 offset1:186
	v_max3_f32 v2, v2, v12, v11
	s_waitcnt lgkmcnt(0)
; #define LAS __attribute__((address_space(3)))
; __device__ __forceinline__ float sum_x32(float v) { const unsigned u = __builtin_bit_cast(unsigned, v); auto rr = __builtin_amdgcn_permlane32_swap(u, u, false, false); return __builtin_bit_cast(float, (unsigned)rr[0]) + __builtin_bit_cast(float, (unsigned)rr[1]); }
; __device__ __forceinline__ float max_x32(float v) { const unsigned u = __builtin_bit_cast(unsigned, v); auto rr = __builtin_amdgcn_permlane32_swap(u, u, false, false); return fmaxf(__builtin_bit_cast(float, (unsigned)rr[0]), __builtin_bit_cast(float, (unsigned)rr[1])); }
; __device__ __forceinline__ unsigned cvt_pk_bf16(float lo, float hi) { unsigned r; asm volatile("v_cvt_pk_bf16_f32 %0, %1, %2" : "=v"(r) : "v"(lo), "v"(hi)); return r; }
; __device__ __forceinline__ s16x4 vtr(const LAS unsigned char* p) { return __builtin_bit_cast(s16x4, __builtin_amdgcn_ds_read_tr16_b64_v4i16((LAS s16x4*)p)); }
; __device__ __forceinline__ void attn_phase(LAS unsigned char* lds, const bf16* U, bf16* YA, const float* sinks, const float* rel_bias, int G, int c, int wbase, int y8) {
;     ...
;             mx = max_x32(mx);
;             float l = 0.f;
; #pragma unroll
;             for (int jt = 0; jt < 5; ++jt)
; #pragma unroll
;                 for (int r = 0; r < 16; ++r) { const float e = __builtin_amdgcn_exp2f(p[jt][r] - mx); p[jt][r] = e; l += e; }
;             l = sum_x32(l); l += __builtin_amdgcn_exp2f(sink2 - mx);
;             f32x16 o[2]; o[0] = (f32x16){}; o[1] = (f32x16){};
;             const LAS unsigned char* vb = lds + VIMG + ((lane >> 4) & 1) * 32 + (lane & 3) * 8 + (4 * hi + ((lane & 15) >> 2)) * 64;
; #pragma unroll
;             for (int jt = 0; jt < 5; ++jt)
; #pragma unroll
;                 for (int s = 0; s < 2; ++s) { u32x4 w; w.x = cvt_pk_bf16(p[jt][8 * s], p[jt][8 * s + 1]); w.y = cvt_pk_bf16(p[jt][8 * s + 2], p[jt][8 * s + 3]); w.z = cvt_pk_bf16(p[jt][8 * s + 4], p[jt][8 * s + 5]); w.w = cvt_pk_bf16(p[jt][8 * s + 6], p[jt][8 * s + 7]);
;                     const bf16x8 pa = __builtin_bit_cast(bf16x8, w);
; #pragma unroll
;                     for (int d0 = 0; d0 < 2; ++d0) { const LAS unsigned char* vp = vb + d0 * 16384 + (32 * (kt0 + jt) + 16 * s) * 64; const s16x4 lo = vtr(vp), hv = vtr(vp + 8 * 64);
;                         const bf16x8 vf = (bf16x8){lo[0], lo[1], lo[2], lo[3], hv[0], hv[1], hv[2], hv[3]};
	v_add_f32_e32 v14, v14, v0
	v_add_f32_e32 v13, v15, v1
	v_max3_f32 v0, v2, v14, v13
	v_mov_b32_e32 v1, v0
	s_nop 1
	v_permlane32_swap_b32_e32 v0, v1
	v_max_f32_e32 v1, v1, v1
	v_max_f32_e32 v0, v0, v0
	v_max_f32_e32 v32, v0, v1
	v_sub_f32_e32 v0, v96, v32
	v_exp_f32_e32 v0, v0
	v_sub_f32_e32 v1, v64, v32
	v_exp_f32_e32 v1, v1
	v_sub_f32_e32 v64, v71, v32
	v_add_f32_e32 v2, 0, v0
	v_exp_f32_e32 v64, v64
	v_add_f32_e32 v3, v1, v2
	v_sub_f32_e32 v2, v66, v32
	v_exp_f32_e32 v2, v2
	v_sub_f32_e32 v48, v48, v32
	v_sub_f32_e32 v33, v33, v32
	v_sub_f32_e32 v16, v16, v32
	v_add_f32_e32 v4, v2, v3
	v_sub_f32_e32 v3, v65, v32
	v_exp_f32_e32 v3, v3
	v_sub_f32_e32 v65, v69, v32
	v_exp_f32_e32 v66, v65
	v_sub_f32_e32 v65, v73, v32
	v_add_f32_e32 v5, v3, v4
	v_sub_f32_e32 v4, v68, v32
	v_exp_f32_e32 v4, v4
	v_exp_f32_e32 v68, v65
	v_sub_f32_e32 v65, v72, v32
	v_exp_f32_e32 v72, v65
	v_add_f32_e32 v6, v4, v5
	v_sub_f32_e32 v5, v67, v32
	v_exp_f32_e32 v5, v5
	v_sub_f32_e32 v65, v75, v32
	v_exp_f32_e32 v75, v65
	v_sub_f32_e32 v65, v74, v32
	v_add_f32_e32 v7, v5, v6
	v_sub_f32_e32 v6, v97, v32
	v_exp_f32_e32 v6, v6
	v_exp_f32_e32 v97, v65
	v_sub_f32_e32 v65, v78, v32
	v_exp_f32_e32 v102, v65
	v_add_f32_e32 v15, v6, v7
	v_sub_f32_e32 v7, v70, v32
	v_exp_f32_e32 v7, v7
	v_sub_f32_e32 v65, v76, v32
	v_exp_f32_e32 v162, v65
	v_sub_f32_e32 v65, v77, v32
	v_add_f32_e32 v15, v7, v15
	v_add_f32_e32 v15, v64, v15
	v_add_f32_e32 v15, v66, v15
	v_add_f32_e32 v15, v68, v15
	v_add_f32_e32 v15, v72, v15
	v_add_f32_e32 v15, v75, v15
	v_exp_f32_e32 v65, v65
	v_add_f32_e32 v15, v97, v15
	v_exp_f32_e32 v67, v48
	v_sub_f32_e32 v48, v50, v32
	v_add_f32_e32 v15, v102, v15
	v_exp_f32_e32 v70, v48
	v_sub_f32_e32 v48, v49, v32
	v_add_f32_e32 v15, v162, v15
	v_exp_f32_e32 v76, v48
	v_sub_f32_e32 v48, v52, v32
	v_add_f32_e32 v15, v65, v15
	v_exp_f32_e32 v96, v48
	v_sub_f32_e32 v48, v51, v32
	v_add_f32_e32 v15, v67, v15
	v_exp_f32_e32 v101, v48
	v_sub_f32_e32 v48, v79, v32
	v_add_f32_e32 v15, v70, v15
	v_exp_f32_e32 v156, v48
	v_sub_f32_e32 v48, v54, v32
	v_add_f32_e32 v15, v76, v15
	v_exp_f32_e32 v166, v48
	v_sub_f32_e32 v48, v55, v32
	v_add_f32_e32 v15, v96, v15
	v_exp_f32_e32 v55, v48
	v_sub_f32_e32 v48, v53, v32
	v_add_f32_e32 v15, v101, v15
	v_exp_f32_e32 v69, v48
	v_sub_f32_e32 v48, v57, v32
	v_add_f32_e32 v15, v156, v15
	v_exp_f32_e32 v71, v48
	v_sub_f32_e32 v48, v56, v32
	v_add_f32_e32 v15, v166, v15
	v_exp_f32_e32 v79, v48
	v_sub_f32_e32 v48, v59, v32
	v_add_f32_e32 v15, v55, v15
	v_exp_f32_e32 v99, v48
	v_sub_f32_e32 v48, v58, v32
	v_add_f32_e32 v15, v69, v15
	v_exp_f32_e32 v105, v48
	v_sub_f32_e32 v48, v62, v32
	v_add_f32_e32 v15, v71, v15
	v_exp_f32_e32 v161, v48
	v_sub_f32_e32 v48, v60, v32
	v_add_f32_e32 v15, v79, v15
	v_exp_f32_e32 v168, v48
	v_sub_f32_e32 v48, v61, v32
	v_add_f32_e32 v15, v99, v15
	v_exp_f32_e32 v59, v48
	v_add_f32_e32 v15, v105, v15
	v_exp_f32_e32 v62, v33
	v_sub_f32_e32 v33, v63, v32
	v_add_f32_e32 v15, v161, v15
	v_exp_f32_e32 v74, v33
	v_sub_f32_e32 v33, v34, v32
	v_add_f32_e32 v15, v168, v15
	v_exp_f32_e32 v100, v33
	v_sub_f32_e32 v33, v36, v32
	v_add_f32_e32 v15, v59, v15
	v_exp_f32_e32 v104, v33
	v_sub_f32_e32 v33, v35, v32
	v_add_f32_e32 v15, v62, v15
	v_exp_f32_e32 v159, v33
	v_sub_f32_e32 v33, v98, v32
	v_add_f32_e32 v15, v74, v15
	v_exp_f32_e32 v165, v33
	v_sub_f32_e32 v33, v38, v32
	v_add_f32_e32 v15, v100, v15
	v_exp_f32_e32 v169, v33
	v_sub_f32_e32 v33, v39, v32
	v_add_f32_e32 v15, v104, v15
	v_exp_f32_e32 v61, v33
	v_sub_f32_e32 v33, v37, v32
	v_add_f32_e32 v15, v159, v15
	v_exp_f32_e32 v73, v33
	v_sub_f32_e32 v33, v41, v32
	v_add_f32_e32 v15, v165, v15
	v_exp_f32_e32 v78, v33
	v_sub_f32_e32 v33, v40, v32
	v_add_f32_e32 v15, v169, v15
	v_exp_f32_e32 v103, v33
	v_sub_f32_e32 v33, v43, v32
	v_add_f32_e32 v15, v61, v15
	v_exp_f32_e32 v157, v33
	v_sub_f32_e32 v33, v42, v32
	v_add_f32_e32 v15, v73, v15
	v_exp_f32_e32 v164, v33
	v_sub_f32_e32 v33, v46, v32
	v_add_f32_e32 v15, v78, v15
	v_exp_f32_e32 v167, v33
	v_sub_f32_e32 v33, v44, v32
	v_add_f32_e32 v15, v103, v15
	v_exp_f32_e32 v170, v33
	v_sub_f32_e32 v33, v45, v32
	v_add_f32_e32 v15, v157, v15
	v_exp_f32_e32 v63, v33
	v_add_f32_e32 v15, v164, v15
	v_exp_f32_e32 v77, v16
	v_sub_f32_e32 v16, v18, v32
	v_add_f32_e32 v15, v167, v15
	v_exp_f32_e32 v98, v16
	v_sub_f32_e32 v16, v17, v32
	v_add_f32_e32 v15, v170, v15
	v_exp_f32_e32 v106, v16
	v_sub_f32_e32 v16, v20, v32
	v_add_f32_e32 v15, v63, v15
	v_exp_f32_e32 v107, v16
	v_sub_f32_e32 v16, v19, v32
	v_add_f32_e32 v15, v77, v15
	v_exp_f32_e32 v158, v16
	v_sub_f32_e32 v16, v22, v32
	v_add_f32_e32 v15, v98, v15
	v_exp_f32_e32 v160, v16
	v_sub_f32_e32 v16, v21, v32
	v_add_f32_e32 v15, v106, v15
	v_exp_f32_e32 v163, v16
	v_sub_f32_e32 v16, v24, v32
	v_add_f32_e32 v15, v107, v15
	v_exp_f32_e32 v51, v16
	v_sub_f32_e32 v16, v23, v32
	v_add_f32_e32 v15, v158, v15
	v_exp_f32_e32 v52, v16
	v_sub_f32_e32 v16, v26, v32
	v_add_f32_e32 v15, v160, v15
	v_exp_f32_e32 v53, v16
	v_sub_f32_e32 v16, v25, v32
	v_add_f32_e32 v15, v163, v15
	v_exp_f32_e32 v54, v16
	v_sub_f32_e32 v16, v28, v32
	v_add_f32_e32 v15, v51, v15
	v_exp_f32_e32 v56, v16
	v_sub_f32_e32 v16, v27, v32
	v_add_f32_e32 v15, v52, v15
	v_exp_f32_e32 v57, v16
	v_sub_f32_e32 v16, v30, v32
	v_add_f32_e32 v15, v53, v15
	v_exp_f32_e32 v58, v16
	v_sub_f32_e32 v16, v29, v32
	v_add_f32_e32 v15, v54, v15
	v_exp_f32_e32 v60, v16
	v_sub_f32_e32 v16, v47, v32
	v_add_f32_e32 v15, v56, v15
	v_exp_f32_e32 v43, v16
	v_sub_f32_e32 v16, v31, v32
	v_add_f32_e32 v15, v57, v15
	v_exp_f32_e32 v44, v16
	v_sub_f32_e32 v16, v172, v32
	v_add_f32_e32 v15, v58, v15
	v_exp_f32_e32 v45, v16
	v_sub_f32_e32 v16, v171, v32
	v_add_f32_e32 v15, v60, v15
	v_exp_f32_e32 v46, v16
	v_sub_f32_e32 v16, v174, v32
	v_add_f32_e32 v15, v43, v15
	v_exp_f32_e32 v47, v16
	v_sub_f32_e32 v16, v173, v32
	v_add_f32_e32 v15, v44, v15
	v_exp_f32_e32 v48, v16
	v_sub_f32_e32 v16, v176, v32
	v_add_f32_e32 v15, v45, v15
	v_exp_f32_e32 v49, v16
	v_sub_f32_e32 v16, v175, v32
	v_add_f32_e32 v15, v46, v15
	v_exp_f32_e32 v50, v16
	v_sub_f32_e32 v16, v177, v32
	v_add_f32_e32 v15, v47, v15
	v_exp_f32_e32 v35, v16
	v_sub_f32_e32 v8, v8, v32
	v_add_f32_e32 v15, v48, v15
	v_exp_f32_e32 v36, v8
	v_sub_f32_e32 v10, v10, v32
	v_add_f32_e32 v15, v49, v15
	v_exp_f32_e32 v37, v10
	v_sub_f32_e32 v9, v9, v32
	v_add_f32_e32 v15, v50, v15
	v_exp_f32_e32 v38, v9
	v_sub_f32_e32 v9, v12, v32
	v_add_f32_e32 v15, v35, v15
	v_exp_f32_e32 v39, v9
	v_sub_f32_e32 v9, v11, v32
	v_add_f32_e32 v8, v36, v15
	v_exp_f32_e32 v40, v9
	v_sub_f32_e32 v9, v14, v32
	v_add_u32_e32 v171, s82, v125
	v_add_f32_e32 v8, v37, v8
	v_exp_f32_e32 v41, v9
	v_sub_f32_e32 v9, v13, v32
	v_cvt_pk_bf16_f32 v16, v0, v1
	v_cvt_pk_bf16_f32 v17, v2, v3
	v_cvt_pk_bf16_f32 v18, v4, v5
	v_cvt_pk_bf16_f32 v19, v6, v7
	ds_read_b64_tr_b16 v[0:1], v171 offset:32768
	ds_read_b64_tr_b16 v[2:3], v171 offset:33280
	v_add_f32_e32 v8, v38, v8
	v_exp_f32_e32 v42, v9
	v_add_f32_e32 v8, v39, v8
	v_add_f32_e32 v8, v40, v8
	v_add_f32_e32 v8, v41, v8
	v_add_f32_e32 v33, v42, v8
	s_waitcnt lgkmcnt(0)
; #define LAS __attribute__((address_space(3)))
; __device__ __forceinline__ float sum_x32(float v) { const unsigned u = __builtin_bit_cast(unsigned, v); auto rr = __builtin_amdgcn_permlane32_swap(u, u, false, false); return __builtin_bit_cast(float, (unsigned)rr[0]) + __builtin_bit_cast(float, (unsigned)rr[1]); }
; __device__ __forceinline__ unsigned cvt_pk_bf16(float lo, float hi) { unsigned r; asm volatile("v_cvt_pk_bf16_f32 %0, %1, %2" : "=v"(r) : "v"(lo), "v"(hi)); return r; }
; __device__ __forceinline__ s16x4 vtr(const LAS unsigned char* p) { return __builtin_bit_cast(s16x4, __builtin_amdgcn_ds_read_tr16_b64_v4i16((LAS s16x4*)p)); }
; __device__ __forceinline__ void attn_phase(LAS unsigned char* lds, const bf16* U, bf16* YA, const float* sinks, const float* rel_bias, int G, int c, int wbase, int y8) {
;     ...
;             l = sum_x32(l); l += __builtin_amdgcn_exp2f(sink2 - mx);
;             f32x16 o[2]; o[0] = (f32x16){}; o[1] = (f32x16){};
;             const LAS unsigned char* vb = lds + VIMG + ((lane >> 4) & 1) * 32 + (lane & 3) * 8 + (4 * hi + ((lane & 15) >> 2)) * 64;
; #pragma unroll
;             for (int jt = 0; jt < 5; ++jt)
; #pragma unroll
;                 for (int s = 0; s < 2; ++s) { u32x4 w; w.x = cvt_pk_bf16(p[jt][8 * s], p[jt][8 * s + 1]); w.y = cvt_pk_bf16(p[jt][8 * s + 2], p[jt][8 * s + 3]); w.z = cvt_pk_bf16(p[jt][8 * s + 4], p[jt][8 * s + 5]); w.w = cvt_pk_bf16(p[jt][8 * s + 6], p[jt][8 * s + 7]);
;                     const bf16x8 pa = __builtin_bit_cast(bf16x8, w);
; #pragma unroll
;                     for (int d0 = 0; d0 < 2; ++d0) { const LAS unsigned char* vp = vb + d0 * 16384 + (32 * (kt0 + jt) + 16 * s) * 64; const s16x4 lo = vtr(vp), hv = vtr(vp + 8 * 64);
;                         const bf16x8 vf = (bf16x8){lo[0], lo[1], lo[2], lo[3], hv[0], hv[1], hv[2], hv[3]};
;                         o[d0] = __builtin_amdgcn_mfma_f32_32x32x16_bf16(pa, vf, o[d0], 0, 0, 0); } }
;             if (hi == 0) lscr[r32] = l;
	v_mfma_f32_32x32x16_bf16 v[0:15], v[16:19], v[0:3], 0
	ds_read_b64_tr_b16 v[20:21], v171 offset:49152
	ds_read_b64_tr_b16 v[22:23], v171 offset:49664
	v_cvt_pk_bf16_f32 v172, v64, v66
	v_cvt_pk_bf16_f32 v173, v68, v72
	v_cvt_pk_bf16_f32 v174, v75, v97
	v_cvt_pk_bf16_f32 v175, v102, v162
	ds_read_b64_tr_b16 v[176:177], v171 offset:33792
	ds_read_b64_tr_b16 v[178:179], v171 offset:34304
	v_add_u32_e32 v102, s12, v125
	s_waitcnt lgkmcnt(2)
	v_mfma_f32_32x32x16_bf16 v[16:31], v[16:19], v[20:23], 0
	v_mov_b32_e32 v34, v33
	s_nop 1
	v_permlane32_swap_b32_e32 v33, v34
	s_waitcnt lgkmcnt(0)
	v_mfma_f32_32x32x16_bf16 v[0:15], v[172:175], v[176:179], v[0:15]
	ds_read_b64_tr_b16 v[176:177], v171 offset:50176
	ds_read_b64_tr_b16 v[178:179], v171 offset:50688
	v_cvt_pk_bf16_f32 v64, v65, v67
	v_cvt_pk_bf16_f32 v65, v70, v76
	v_cvt_pk_bf16_f32 v66, v96, v101
	v_add_u32_e32 v101, s83, v125
	v_cvt_pk_bf16_f32 v67, v156, v166
	s_waitcnt lgkmcnt(0)
	v_mfma_f32_32x32x16_bf16 v[16:31], v[172:175], v[176:179], v[16:31]
	ds_read_b64_tr_b16 v[172:173], v101 offset:32768
	ds_read_b64_tr_b16 v[174:175], v101 offset:33280
	s_waitcnt lgkmcnt(0)
	v_mfma_f32_32x32x16_bf16 v[0:15], v[64:67], v[172:175], v[0:15]
	ds_read_b64_tr_b16 v[172:173], v101 offset:49152
	ds_read_b64_tr_b16 v[174:175], v101 offset:49664
	s_waitcnt lgkmcnt(0)
	v_mfma_f32_32x32x16_bf16 v[16:31], v[64:67], v[172:175], v[16:31]
	v_cvt_pk_bf16_f32 v64, v55, v69
	v_cvt_pk_bf16_f32 v65, v71, v79
	v_cvt_pk_bf16_f32 v66, v99, v105
	v_cvt_pk_bf16_f32 v67, v161, v168
	ds_read_b64_tr_b16 v[68:69], v101 offset:33792
	ds_read_b64_tr_b16 v[70:71], v101 offset:34304
	s_waitcnt lgkmcnt(0)
	v_mfma_f32_32x32x16_bf16 v[0:15], v[64:67], v[68:71], v[0:15]
	ds_read_b64_tr_b16 v[68:69], v101 offset:50176
	ds_read_b64_tr_b16 v[70:71], v101 offset:50688
	s_waitcnt lgkmcnt(0)
	v_mfma_f32_32x32x16_bf16 v[16:31], v[64:67], v[68:71], v[16:31]
	v_cvt_pk_bf16_f32 v64, v59, v62
	v_cvt_pk_bf16_f32 v65, v74, v100
	v_cvt_pk_bf16_f32 v66, v104, v159
	v_cvt_pk_bf16_f32 v67, v165, v169
	ds_read_b64_tr_b16 v[68:69], v102 offset:32768
	ds_read_b64_tr_b16 v[70:71], v102 offset:33280
	v_add_u32_e32 v104, s56, v125
	s_waitcnt lgkmcnt(0)
	v_mfma_f32_32x32x16_bf16 v[0:15], v[64:67], v[68:71], v[0:15]
	ds_read_b64_tr_b16 v[68:69], v102 offset:49152
	ds_read_b64_tr_b16 v[70:71], v102 offset:49664
	s_waitcnt lgkmcnt(0)
	v_mfma_f32_32x32x16_bf16 v[16:31], v[64:67], v[68:71], v[16:31]
	v_cvt_pk_bf16_f32 v64, v61, v73
	v_cvt_pk_bf16_f32 v65, v78, v103
	v_cvt_pk_bf16_f32 v66, v157, v164
	v_cvt_pk_bf16_f32 v67, v167, v170
	ds_read_b64_tr_b16 v[68:69], v102 offset:33792
	ds_read_b64_tr_b16 v[70:71], v102 offset:34304
	v_add_u32_e32 v103, s13, v125
	s_waitcnt lgkmcnt(0)
	v_mfma_f32_32x32x16_bf16 v[0:15], v[64:67], v[68:71], v[0:15]
	ds_read_b64_tr_b16 v[68:69], v102 offset:50176
	ds_read_b64_tr_b16 v[70:71], v102 offset:50688
	v_cvt_pk_bf16_f32 v62, v63, v77
	v_cvt_pk_bf16_f32 v63, v98, v106
	s_waitcnt lgkmcnt(0)
	v_mfma_f32_32x32x16_bf16 v[16:31], v[64:67], v[68:71], v[16:31]
	v_cvt_pk_bf16_f32 v64, v107, v158
	v_cvt_pk_bf16_f32 v65, v160, v163
	ds_read_b64_tr_b16 v[66:67], v103 offset:32768
	ds_read_b64_tr_b16 v[68:69], v103 offset:33280
	s_waitcnt lgkmcnt(0)
	v_mfma_f32_32x32x16_bf16 v[0:15], v[62:65], v[66:69], v[0:15]
	ds_read_b64_tr_b16 v[66:67], v103 offset:49152
	ds_read_b64_tr_b16 v[68:69], v103 offset:49664
	v_cvt_pk_bf16_f32 v52, v51, v52
	v_cvt_pk_bf16_f32 v53, v53, v54
	v_cvt_pk_bf16_f32 v54, v56, v57
	v_cvt_pk_bf16_f32 v55, v58, v60
	ds_read_b64_tr_b16 v[56:57], v103 offset:33792
	ds_read_b64_tr_b16 v[58:59], v103 offset:34304
	s_waitcnt lgkmcnt(2)
	v_mfma_f32_32x32x16_bf16 v[16:31], v[62:65], v[66:69], v[16:31]
	s_waitcnt lgkmcnt(0)
	v_mfma_f32_32x32x16_bf16 v[0:15], v[52:55], v[56:59], v[0:15]
	ds_read_b64_tr_b16 v[56:57], v103 offset:50176
	ds_read_b64_tr_b16 v[58:59], v103 offset:50688
	v_cvt_pk_bf16_f32 v44, v43, v44
	v_cvt_pk_bf16_f32 v45, v45, v46
	v_cvt_pk_bf16_f32 v46, v47, v48
	v_cvt_pk_bf16_f32 v47, v49, v50
	ds_read_b64_tr_b16 v[48:49], v104 offset:32768
	ds_read_b64_tr_b16 v[50:51], v104 offset:33280
	s_waitcnt lgkmcnt(2)
	v_mfma_f32_32x32x16_bf16 v[16:31], v[52:55], v[56:59], v[16:31]
	s_waitcnt lgkmcnt(0)
	v_mfma_f32_32x32x16_bf16 v[0:15], v[44:47], v[48:51], v[0:15]
	ds_read_b64_tr_b16 v[48:49], v104 offset:49152
	ds_read_b64_tr_b16 v[50:51], v104 offset:49664
	v_cvt_pk_bf16_f32 v36, v35, v36
	v_cvt_pk_bf16_f32 v37, v37, v38
	v_cvt_pk_bf16_f32 v38, v39, v40
	v_cvt_pk_bf16_f32 v39, v41, v42
	ds_read_b64_tr_b16 v[40:41], v104 offset:33792
	ds_read_b64_tr_b16 v[42:43], v104 offset:34304
	s_waitcnt lgkmcnt(2)
	v_mfma_f32_32x32x16_bf16 v[16:31], v[44:47], v[48:51], v[16:31]
	s_waitcnt lgkmcnt(0)
	v_mfma_f32_32x32x16_bf16 v[0:15], v[36:39], v[40:43], v[0:15]
	ds_read_b64_tr_b16 v[40:41], v104 offset:50176
	ds_read_b64_tr_b16 v[42:43], v104 offset:50688
	s_waitcnt lgkmcnt(0)
	v_mfma_f32_32x32x16_bf16 v[16:31], v[36:39], v[40:43], v[16:31]
	s_and_saveexec_b64 s[30:31], s[2:3]
	s_cbranch_execz .LBB0_556
	v_sub_f32_e32 v32, v151, v32
	v_exp_f32_e32 v32, v32
	v_add_f32_e32 v33, v33, v34
	v_add_f32_e32 v32, v33, v32
	ds_write_b32 v126, v32

; #define LAS __attribute__((address_space(3)))
; __device__ __forceinline__ int crow(int r, int hi) { return (r & 3) + 8 * (r >> 2) + 4 * hi; }
; __device__ __forceinline__ int crow(int r, int hi) { return (r & 3) + 8 * (r >> 2) + 4 * hi; }
; __device__ __forceinline__ void attn_phase(LAS unsigned char* lds, const bf16* U, bf16* YA, const float* sinks, const float* rel_bias, int G, int c, int wbase, int y8) {
;     ...
;         for (int qt = 0; qt < 2; ++qt) {
;             const int iq0 = 64 * qh + 32 * qt, kt0 = iq0 >> 5; const size_t mq = mq0 + 32 * qt;
;             f32x16 p[5];
; #pragma unroll
;             for (int jt = 0; jt < 5; ++jt) { f32x16 a = {};
; #pragma unroll
;                 for (int d0 = 0; d0 < 4; ++d0) { const bf16x8 kf = *(const LAS bf16x8*)(lds + KIMG + (2 * d0 + hi) * 4096 + (32 * (kt0 + jt) + r32) * 16); a = __builtin_amdgcn_mfma_f32_32x32x16_bf16(kf, qf[qt][d0], a, 0, 0, 0); }
;                 p[jt] = a; }
;             float mx = sink2;
; #pragma unroll
;             for (int jt = 0; jt < 5; ++jt)
; #pragma unroll
;                 for (int r = 0; r < 16; ++r) { float s = p[jt][r] + bt[32 * jt + (r & 3) + 8 * (r >> 2)];
;                     if (n == 0) { if (32 * (kt0 + jt) + crow(r, hi) < 128) s = -1.0e30f; }
;                     p[jt][r] = s; mx = fmaxf(mx, s); }
.LBB0_568:
	s_waitcnt lgkmcnt(0)
	s_waitcnt lgkmcnt(0)
	ds_read_b128 v[180:183], v152
	ds_read_b128 v[184:187], v152 offset:8192
	ds_read_b128 v[188:191], v152 offset:16384
	ds_read_b128 v[192:195], v152 offset:24576
	v_add_u32_e32 v105, s57, v123
	s_waitcnt lgkmcnt(3)
	v_mfma_f32_32x32x16_bf16 v[64:79], v[180:183], v[92:95], 0
	ds_read_b128 v[180:183], v153
	s_waitcnt lgkmcnt(3)
	v_mfma_f32_32x32x16_bf16 v[64:79], v[184:187], v[88:91], v[64:79]
	ds_read_b128 v[184:187], v153 offset:8192
	s_waitcnt lgkmcnt(3)
	v_mfma_f32_32x32x16_bf16 v[64:79], v[188:191], v[84:87], v[64:79]
	ds_read_b128 v[188:191], v153 offset:16384
	s_waitcnt lgkmcnt(3)
	v_mfma_f32_32x32x16_bf16 v[64:79], v[192:195], v[80:83], v[64:79]
	ds_read_b128 v[192:195], v153 offset:24576
	s_waitcnt lgkmcnt(3)
	v_mfma_f32_32x32x16_bf16 v[48:63], v[180:183], v[92:95], 0
	ds_read_b128 v[180:183], v154
	s_waitcnt lgkmcnt(3)
	v_mfma_f32_32x32x16_bf16 v[48:63], v[184:187], v[88:91], v[48:63]
	ds_read_b128 v[184:187], v154 offset:8192
	s_waitcnt lgkmcnt(3)
	v_mfma_f32_32x32x16_bf16 v[48:63], v[188:191], v[84:87], v[48:63]
	ds_read_b128 v[188:191], v154 offset:16384
	s_waitcnt lgkmcnt(3)
	v_mfma_f32_32x32x16_bf16 v[48:63], v[192:195], v[80:83], v[48:63]
	ds_read_b128 v[192:195], v154 offset:24576
	s_waitcnt lgkmcnt(3)
	v_mfma_f32_32x32x16_bf16 v[32:47], v[180:183], v[92:95], 0
	ds_read_b128 v[180:183], v155
	s_waitcnt lgkmcnt(3)
	v_mfma_f32_32x32x16_bf16 v[32:47], v[184:187], v[88:91], v[32:47]
	ds_read_b128 v[184:187], v155 offset:8192
	s_waitcnt lgkmcnt(3)
	v_mfma_f32_32x32x16_bf16 v[32:47], v[188:191], v[84:87], v[32:47]
	ds_read_b128 v[188:191], v155 offset:16384
	s_waitcnt lgkmcnt(3)
	v_mfma_f32_32x32x16_bf16 v[32:47], v[192:195], v[80:83], v[32:47]
	ds_read_b128 v[192:195], v155 offset:24576
	s_waitcnt lgkmcnt(3)
	v_mfma_f32_32x32x16_bf16 v[16:31], v[180:183], v[92:95], 0
	ds_read_b128 v[180:183], v105
	s_waitcnt lgkmcnt(3)
	v_mfma_f32_32x32x16_bf16 v[16:31], v[184:187], v[88:91], v[16:31]
	ds_read_b128 v[184:187], v105 offset:8192
	s_waitcnt lgkmcnt(3)
	v_mfma_f32_32x32x16_bf16 v[16:31], v[188:191], v[84:87], v[16:31]
	ds_read_b128 v[188:191], v105 offset:16384
	s_waitcnt lgkmcnt(3)
	v_mfma_f32_32x32x16_bf16 v[16:31], v[192:195], v[80:83], v[16:31]
	ds_read_b128 v[192:195], v105 offset:24576
	s_waitcnt lgkmcnt(3)
	v_mfma_f32_32x32x16_bf16 v[0:15], v[180:183], v[92:95], 0
	s_waitcnt lgkmcnt(2)
	v_mfma_f32_32x32x16_bf16 v[0:15], v[184:187], v[88:91], v[0:15]
	s_waitcnt lgkmcnt(1)
	v_mfma_f32_32x32x16_bf16 v[0:15], v[188:191], v[84:87], v[0:15]
	s_waitcnt lgkmcnt(0)
	v_mfma_f32_32x32x16_bf16 v[0:15], v[192:195], v[80:83], v[0:15]
	ds_read2_b32 v[80:81], v121 offset0:31 offset1:32
	ds_read2_b32 v[82:83], v121 offset0:33 offset1:34
	v_mov_b32_e32 v86, 0xf149f2ca
	s_waitcnt lgkmcnt(1)
	v_add_f32_e32 v64, v64, v80
	v_cndmask_b32_e64 v80, v64, v86, s[4:5]
	v_add_f32_e32 v64, v65, v81
	s_waitcnt lgkmcnt(0)
	v_add_f32_e32 v65, v66, v82
	v_cndmask_b32_e64 v66, v65, v86, s[4:5]
	v_add_f32_e32 v65, v67, v83
	ds_read2_b32 v[82:83], v121 offset0:39 offset1:40
	v_cndmask_b32_e64 v64, v64, v86, s[4:5]
	v_max3_f32 v81, v151, v80, v64
	v_cndmask_b32_e64 v65, v65, v86, s[4:5]
	v_max3_f32 v81, v81, v66, v65
	s_waitcnt lgkmcnt(0)
	v_add_f32_e32 v67, v68, v82
	v_cndmask_b32_e64 v68, v67, v86, s[4:5]
	v_add_f32_e32 v67, v69, v83
	ds_read2_b32 v[82:83], v121 offset0:41 offset1:42
	v_cndmask_b32_e64 v67, v67, v86, s[4:5]
	v_max3_f32 v69, v81, v68, v67
	s_waitcnt lgkmcnt(0)
	v_add_f32_e32 v70, v70, v82
	v_cndmask_b32_e64 v81, v70, v86, s[4:5]
	v_add_f32_e32 v70, v71, v83
	ds_read2_b32 v[82:83], v121 offset0:47 offset1:48
	v_cndmask_b32_e64 v70, v70, v86, s[4:5]
	v_max3_f32 v84, v69, v81, v70
	s_waitcnt lgkmcnt(0)
	v_add_f32_e32 v69, v72, v82
	v_cndmask_b32_e64 v71, v69, v86, s[4:5]
	v_add_f32_e32 v69, v73, v83
	ds_read2_b32 v[82:83], v121 offset0:49 offset1:50
	v_cndmask_b32_e64 v69, v69, v86, s[4:5]
	v_max3_f32 v84, v84, v71, v69
	s_waitcnt lgkmcnt(0)
	v_add_f32_e32 v72, v74, v82
	v_cndmask_b32_e64 v73, v72, v86, s[4:5]
	v_add_f32_e32 v72, v75, v83
	ds_read2_b32 v[82:83], v121 offset0:55 offset1:56
	v_cndmask_b32_e64 v72, v72, v86, s[4:5]
	v_max3_f32 v84, v84, v73, v72
	s_waitcnt lgkmcnt(0)
	v_add_f32_e32 v74, v76, v82
	v_cndmask_b32_e64 v75, v74, v86, s[4:5]
	v_add_f32_e32 v74, v77, v83
	ds_read2_b32 v[76:77], v121 offset0:57 offset1:58
	v_cndmask_b32_e64 v74, v74, v86, s[4:5]
	v_max3_f32 v82, v84, v75, v74
	s_waitcnt lgkmcnt(0)
	v_add_f32_e32 v76, v78, v76
	v_cndmask_b32_e64 v78, v76, v86, s[4:5]
	v_add_f32_e32 v76, v79, v77
	v_cndmask_b32_e64 v76, v76, v86, s[4:5]
	v_max3_f32 v79, v82, v78, v76
	ds_read2_b32 v[82:83], v121 offset0:63 offset1:64
	s_waitcnt lgkmcnt(0)
	v_add_f32_e32 v48, v48, v82
	v_cndmask_b32_e64 v77, v48, v86, s[6:7]
	v_add_f32_e32 v48, v49, v83
	ds_read2_b32 v[82:83], v121 offset0:65 offset1:66
	v_cndmask_b32_e64 v48, v48, v86, s[6:7]
	v_max3_f32 v79, v79, v77, v48
	s_waitcnt lgkmcnt(0)
	v_add_f32_e32 v49, v50, v82
	v_cndmask_b32_e64 v50, v49, v86, s[6:7]
	v_add_f32_e32 v49, v51, v83
	ds_read2_b32 v[82:83], v121 offset0:71 offset1:72
	v_cndmask_b32_e64 v49, v49, v86, s[6:7]
	v_max3_f32 v79, v79, v50, v49
	s_waitcnt lgkmcnt(0)
	v_add_f32_e32 v51, v52, v82
	v_cndmask_b32_e64 v52, v51, v86, s[6:7]
	v_add_f32_e32 v51, v53, v83
	ds_read2_b32 v[82:83], v121 offset0:73 offset1:74
	v_cndmask_b32_e64 v51, v51, v86, s[6:7]
	v_max3_f32 v53, v79, v52, v51
	s_waitcnt lgkmcnt(0)
	v_add_f32_e32 v54, v54, v82
	v_cndmask_b32_e64 v79, v54, v86, s[6:7]
	v_add_f32_e32 v54, v55, v83
	ds_read2_b32 v[82:83], v121 offset0:79 offset1:80
	v_cndmask_b32_e64 v54, v54, v86, s[6:7]
	v_max3_f32 v84, v53, v79, v54
	s_waitcnt lgkmcnt(0)
; __device__ __forceinline__ int crow(int r, int hi) { return (r & 3) + 8 * (r >> 2) + 4 * hi; }
; __device__ __forceinline__ int crow(int r, int hi) { return (r & 3) + 8 * (r >> 2) + 4 * hi; }
; __device__ __forceinline__ void attn_phase(LAS unsigned char* lds, const bf16* U, bf16* YA, const float* sinks, const float* rel_bias, int G, int c, int wbase, int y8) {
;     ...
;             float mx = sink2;
; #pragma unroll
;             for (int jt = 0; jt < 5; ++jt)
; #pragma unroll
;                 for (int r = 0; r < 16; ++r) { float s = p[jt][r] + bt[32 * jt + (r & 3) + 8 * (r >> 2)];
;                     if (n == 0) { if (32 * (kt0 + jt) + crow(r, hi) < 128) s = -1.0e30f; }
;                     p[jt][r] = s; mx = fmaxf(mx, s); }
	v_add_f32_e32 v53, v56, v82
	v_cndmask_b32_e64 v55, v53, v86, s[6:7]
	v_add_f32_e32 v53, v57, v83
	ds_read2_b32 v[82:83], v121 offset0:81 offset1:82
	v_cndmask_b32_e64 v53, v53, v86, s[6:7]
	v_max3_f32 v84, v84, v55, v53
	s_waitcnt lgkmcnt(0)
	v_add_f32_e32 v56, v58, v82
	v_cndmask_b32_e64 v57, v56, v86, s[6:7]
	v_add_f32_e32 v56, v59, v83
	ds_read2_b32 v[82:83], v121 offset0:87 offset1:88
	v_cndmask_b32_e64 v56, v56, v86, s[6:7]
	v_max3_f32 v84, v84, v57, v56
	s_waitcnt lgkmcnt(0)
	v_add_f32_e32 v58, v60, v82
	v_cndmask_b32_e64 v59, v58, v86, s[6:7]
	v_add_f32_e32 v58, v61, v83
	ds_read2_b32 v[60:61], v121 offset0:89 offset1:90
	v_cndmask_b32_e64 v58, v58, v86, s[6:7]
	v_max3_f32 v82, v84, v59, v58
	ds_read2_b32 v[84:85], v121 offset0:111 offset1:112
	s_waitcnt lgkmcnt(1)
	v_add_f32_e32 v60, v62, v60
	v_cndmask_b32_e64 v62, v60, v86, s[6:7]
	v_add_f32_e32 v60, v63, v61
	v_cndmask_b32_e64 v60, v60, v86, s[6:7]
	v_max3_f32 v63, v82, v62, v60
	ds_read2_b32 v[82:83], v121 offset0:95 offset1:96
	s_waitcnt lgkmcnt(0)
	v_add_f32_e32 v32, v32, v82
	v_cndmask_b32_e64 v61, v32, v86, s[6:7]
	v_add_f32_e32 v32, v33, v83
	ds_read2_b32 v[82:83], v121 offset0:97 offset1:98
	v_cndmask_b32_e64 v33, v32, v86, s[6:7]
	v_max3_f32 v32, v63, v61, v33
	s_waitcnt lgkmcnt(0)
	v_add_f32_e32 v34, v34, v82
	v_cndmask_b32_e64 v63, v34, v86, s[6:7]
	v_add_f32_e32 v34, v35, v83
	ds_read2_b32 v[82:83], v121 offset0:103 offset1:104
	v_cndmask_b32_e64 v34, v34, v86, s[6:7]
	v_max3_f32 v32, v32, v63, v34
	s_waitcnt lgkmcnt(0)
	v_add_f32_e32 v35, v36, v82
	v_cndmask_b32_e64 v36, v35, v86, s[6:7]
	v_add_f32_e32 v35, v37, v83
	ds_read2_b32 v[82:83], v121 offset0:105 offset1:106
	v_cndmask_b32_e64 v35, v35, v86, s[6:7]
	v_max3_f32 v32, v32, v36, v35
	s_waitcnt lgkmcnt(0)
	v_add_f32_e32 v37, v38, v82
	v_add_f32_e32 v38, v40, v84
	v_cndmask_b32_e64 v82, v37, v86, s[6:7]
	v_add_f32_e32 v37, v39, v83
	v_cndmask_b32_e64 v39, v38, v86, s[6:7]
	v_add_f32_e32 v38, v41, v85
	ds_read2_b32 v[84:85], v121 offset0:113 offset1:114
	v_cndmask_b32_e64 v37, v37, v86, s[6:7]
	v_max3_f32 v32, v32, v82, v37
	v_cndmask_b32_e64 v38, v38, v86, s[6:7]
	v_max3_f32 v32, v32, v39, v38
	s_waitcnt lgkmcnt(0)
	v_add_f32_e32 v40, v42, v84
	v_cndmask_b32_e64 v41, v40, v86, s[6:7]
	v_add_f32_e32 v40, v43, v85
	ds_read2_b32 v[84:85], v121 offset0:119 offset1:120
	v_cndmask_b32_e64 v40, v40, v86, s[6:7]
	v_max3_f32 v32, v32, v41, v40
	s_waitcnt lgkmcnt(0)
	v_add_f32_e32 v42, v44, v84
	v_cndmask_b32_e64 v43, v42, v86, s[6:7]
	v_add_f32_e32 v42, v45, v85
	ds_read2_b32 v[44:45], v121 offset0:121 offset1:122
	ds_read2_b32 v[84:85], v121 offset0:127 offset1:128
	v_cndmask_b32_e64 v42, v42, v86, s[6:7]
	v_max3_f32 v32, v32, v43, v42
	s_waitcnt lgkmcnt(1)
	v_add_f32_e32 v44, v46, v44
	v_cndmask_b32_e64 v46, v44, v86, s[6:7]
	v_add_f32_e32 v44, v47, v45
	s_waitcnt lgkmcnt(0)
	v_add_f32_e32 v45, v16, v84
	v_add_f32_e32 v16, v17, v85
	ds_read2_b32 v[84:85], v121 offset0:129 offset1:130
	v_cndmask_b32_e64 v44, v44, v86, s[6:7]
	v_max3_f32 v32, v32, v46, v44
	v_max3_f32 v32, v32, v45, v16
	s_waitcnt lgkmcnt(0)
	v_add_f32_e32 v18, v18, v84
	v_add_f32_e32 v17, v19, v85
	ds_read2_b32 v[84:85], v121 offset0:135 offset1:136
	v_max3_f32 v32, v32, v18, v17
	s_waitcnt lgkmcnt(0)
	v_add_f32_e32 v20, v20, v84
	v_add_f32_e32 v19, v21, v85
	ds_read2_b32 v[84:85], v121 offset0:137 offset1:138
	v_max3_f32 v32, v32, v20, v19
	s_waitcnt lgkmcnt(0)
	v_add_f32_e32 v22, v22, v84
	v_add_f32_e32 v21, v23, v85
	ds_read2_b32 v[84:85], v121 offset0:143 offset1:144
	v_max3_f32 v32, v32, v22, v21
	s_waitcnt lgkmcnt(0)
	v_add_f32_e32 v24, v24, v84
	v_add_f32_e32 v23, v25, v85
	ds_read2_b32 v[84:85], v121 offset0:145 offset1:146
	v_max3_f32 v32, v32, v24, v23
	s_waitcnt lgkmcnt(0)
	v_add_f32_e32 v26, v26, v84
	v_add_f32_e32 v25, v27, v85
	ds_read2_b32 v[84:85], v121 offset0:151 offset1:152
	v_max3_f32 v32, v32, v26, v25
	s_waitcnt lgkmcnt(0)
	v_add_f32_e32 v28, v28, v84
	v_add_f32_e32 v27, v29, v85
	ds_read2_b32 v[84:85], v121 offset0:153 offset1:154
	v_max3_f32 v32, v32, v28, v27
	s_waitcnt lgkmcnt(0)
	v_add_f32_e32 v30, v30, v84
	v_add_f32_e32 v29, v31, v85
	ds_read2_b32 v[84:85], v121 offset0:159 offset1:160
	v_max3_f32 v32, v32, v30, v29
	s_waitcnt lgkmcnt(0)
	v_add_f32_e32 v47, v0, v84
	v_add_f32_e32 v31, v1, v85
	ds_read2_b32 v[0:1], v121 offset0:161 offset1:162
	v_max3_f32 v32, v32, v47, v31
	s_waitcnt lgkmcnt(0)
	v_add_f32_e32 v161, v2, v0
	v_add_f32_e32 v160, v3, v1
	ds_read2_b32 v[0:1], v121 offset0:167 offset1:168
	v_max3_f32 v2, v32, v161, v160
	s_waitcnt lgkmcnt(0)
	v_add_f32_e32 v163, v4, v0
	v_add_f32_e32 v162, v5, v1
	ds_read2_b32 v[0:1], v121 offset0:169 offset1:170
	v_max3_f32 v2, v2, v163, v162
	s_waitcnt lgkmcnt(0)
	v_add_f32_e32 v165, v6, v0
	v_add_f32_e32 v164, v7, v1
	ds_read2_b32 v[0:1], v121 offset0:175 offset1:176
	v_max3_f32 v2, v2, v165, v164
	s_waitcnt lgkmcnt(0)
	v_add_f32_e32 v166, v8, v0
	v_add_f32_e32 v8, v9, v1
	ds_read2_b32 v[0:1], v121 offset0:177 offset1:178
	v_max3_f32 v2, v2, v166, v8
	s_waitcnt lgkmcnt(0)
	v_add_f32_e32 v10, v10, v0
	v_add_f32_e32 v9, v11, v1
	ds_read2_b32 v[0:1], v121 offset0:183 offset1:184
	v_max3_f32 v2, v2, v10, v9
	s_waitcnt lgkmcnt(0)
	v_add_f32_e32 v12, v12, v0
	v_add_f32_e32 v11, v13, v1
	ds_read2_b32 v[0:1], v121 offset0:185 offset1:186
	v_max3_f32 v2, v2, v12, v11
	s_waitcnt lgkmcnt(0)
; #define LAS __attribute__((address_space(3)))
; __device__ __forceinline__ float sum_x32(float v) { const unsigned u = __builtin_bit_cast(unsigned, v); auto rr = __builtin_amdgcn_permlane32_swap(u, u, false, false); return __builtin_bit_cast(float, (unsigned)rr[0]) + __builtin_bit_cast(float, (unsigned)rr[1]); }
; __device__ __forceinline__ float max_x32(float v) { const unsigned u = __builtin_bit_cast(unsigned, v); auto rr = __builtin_amdgcn_permlane32_swap(u, u, false, false); return fmaxf(__builtin_bit_cast(float, (unsigned)rr[0]), __builtin_bit_cast(float, (unsigned)rr[1])); }
; __device__ __forceinline__ unsigned cvt_pk_bf16(float lo, float hi) { unsigned r; asm volatile("v_cvt_pk_bf16_f32 %0, %1, %2" : "=v"(r) : "v"(lo), "v"(hi)); return r; }
; __device__ __forceinline__ s16x4 vtr(const LAS unsigned char* p) { return __builtin_bit_cast(s16x4, __builtin_amdgcn_ds_read_tr16_b64_v4i16((LAS s16x4*)p)); }
; __device__ __forceinline__ void attn_phase(LAS unsigned char* lds, const bf16* U, bf16* YA, const float* sinks, const float* rel_bias, int G, int c, int wbase, int y8) {
;     ...
;             mx = max_x32(mx);
;             float l = 0.f;
; #pragma unroll
;             for (int jt = 0; jt < 5; ++jt)
; #pragma unroll
;                 for (int r = 0; r < 16; ++r) { const float e = __builtin_amdgcn_exp2f(p[jt][r] - mx); p[jt][r] = e; l += e; }
;             l = sum_x32(l); l += __builtin_amdgcn_exp2f(sink2 - mx);
;             f32x16 o[2]; o[0] = (f32x16){}; o[1] = (f32x16){};
;             const LAS unsigned char* vb = lds + VIMG + ((lane >> 4) & 1) * 32 + (lane & 3) * 8 + (4 * hi + ((lane & 15) >> 2)) * 64;
; #pragma unroll
;             for (int jt = 0; jt < 5; ++jt)
; #pragma unroll
;                 for (int s = 0; s < 2; ++s) { u32x4 w; w.x = cvt_pk_bf16(p[jt][8 * s], p[jt][8 * s + 1]); w.y = cvt_pk_bf16(p[jt][8 * s + 2], p[jt][8 * s + 3]); w.z = cvt_pk_bf16(p[jt][8 * s + 4], p[jt][8 * s + 5]); w.w = cvt_pk_bf16(p[jt][8 * s + 6], p[jt][8 * s + 7]);
;                     const bf16x8 pa = __builtin_bit_cast(bf16x8, w);
; #pragma unroll
;                     for (int d0 = 0; d0 < 2; ++d0) { const LAS unsigned char* vp = vb + d0 * 16384 + (32 * (kt0 + jt) + 16 * s) * 64; const s16x4 lo = vtr(vp), hv = vtr(vp + 8 * 64);
;                         const bf16x8 vf = (bf16x8){lo[0], lo[1], lo[2], lo[3], hv[0], hv[1], hv[2], hv[3]};
	v_add_f32_e32 v14, v14, v0
	v_add_f32_e32 v13, v15, v1
	v_max3_f32 v0, v2, v14, v13
	v_mov_b32_e32 v1, v0
	s_nop 1
	v_permlane32_swap_b32_e32 v0, v1
	v_max_f32_e32 v1, v1, v1
	v_max_f32_e32 v0, v0, v0
	v_max_f32_e32 v32, v0, v1
	v_sub_f32_e32 v0, v80, v32
	v_exp_f32_e32 v0, v0
	v_sub_f32_e32 v1, v64, v32
	v_exp_f32_e32 v1, v1
	v_sub_f32_e32 v64, v71, v32
	v_add_f32_e32 v2, 0, v0
	v_exp_f32_e32 v64, v64
	v_add_f32_e32 v3, v1, v2
	v_sub_f32_e32 v2, v66, v32
	v_exp_f32_e32 v2, v2
	v_sub_f32_e32 v48, v48, v32
	v_sub_f32_e32 v33, v33, v32
	v_sub_f32_e32 v16, v16, v32
	v_add_f32_e32 v4, v2, v3
	v_sub_f32_e32 v3, v65, v32
	v_exp_f32_e32 v3, v3
	v_sub_f32_e32 v65, v69, v32
	v_exp_f32_e32 v66, v65
	v_sub_f32_e32 v65, v73, v32
	v_add_f32_e32 v5, v3, v4
	v_sub_f32_e32 v4, v68, v32
	v_exp_f32_e32 v4, v4
	v_exp_f32_e32 v68, v65
	v_sub_f32_e32 v65, v72, v32
	v_exp_f32_e32 v72, v65
	v_add_f32_e32 v6, v4, v5
	v_sub_f32_e32 v5, v67, v32
	v_exp_f32_e32 v5, v5
	v_sub_f32_e32 v65, v75, v32
	v_exp_f32_e32 v75, v65
	v_sub_f32_e32 v65, v74, v32
	v_add_f32_e32 v7, v5, v6
	v_sub_f32_e32 v6, v81, v32
	v_exp_f32_e32 v6, v6
	v_exp_f32_e32 v81, v65
	v_sub_f32_e32 v65, v78, v32
	v_exp_f32_e32 v86, v65
	v_add_f32_e32 v15, v6, v7
	v_sub_f32_e32 v7, v70, v32
	v_exp_f32_e32 v7, v7
	v_sub_f32_e32 v65, v76, v32
	v_exp_f32_e32 v107, v65
	v_sub_f32_e32 v65, v77, v32
	v_add_f32_e32 v15, v7, v15
	v_add_f32_e32 v15, v64, v15
	v_add_f32_e32 v15, v66, v15
	v_add_f32_e32 v15, v68, v15
	v_add_f32_e32 v15, v72, v15
	v_add_f32_e32 v15, v75, v15
	v_exp_f32_e32 v65, v65
	v_add_f32_e32 v15, v81, v15
	v_exp_f32_e32 v67, v48
	v_sub_f32_e32 v48, v50, v32
	v_add_f32_e32 v15, v86, v15
	v_exp_f32_e32 v70, v48
	v_sub_f32_e32 v48, v49, v32
	v_add_f32_e32 v15, v107, v15
	v_exp_f32_e32 v76, v48
	v_sub_f32_e32 v48, v52, v32
	v_add_f32_e32 v15, v65, v15
	v_exp_f32_e32 v80, v48
	v_sub_f32_e32 v48, v51, v32
	v_add_f32_e32 v15, v67, v15
	v_exp_f32_e32 v85, v48
	v_sub_f32_e32 v48, v79, v32
	v_add_f32_e32 v15, v70, v15
	v_exp_f32_e32 v91, v48
	v_sub_f32_e32 v48, v54, v32
	v_add_f32_e32 v15, v76, v15
	v_exp_f32_e32 v155, v48
	v_sub_f32_e32 v48, v55, v32
	v_add_f32_e32 v15, v80, v15
	v_exp_f32_e32 v54, v48
	v_sub_f32_e32 v48, v53, v32
	v_add_f32_e32 v15, v85, v15
	v_exp_f32_e32 v69, v48
	v_sub_f32_e32 v48, v57, v32
	v_add_f32_e32 v15, v91, v15
	v_exp_f32_e32 v71, v48
	v_sub_f32_e32 v48, v56, v32
	v_add_f32_e32 v15, v155, v15
	v_exp_f32_e32 v79, v48
	v_sub_f32_e32 v48, v59, v32
	v_add_f32_e32 v15, v54, v15
	v_exp_f32_e32 v83, v48
	v_sub_f32_e32 v48, v58, v32
	v_add_f32_e32 v15, v69, v15
	v_exp_f32_e32 v89, v48
	v_sub_f32_e32 v48, v62, v32
	v_add_f32_e32 v15, v71, v15
	v_exp_f32_e32 v105, v48
	v_sub_f32_e32 v48, v60, v32
	v_add_f32_e32 v15, v79, v15
	v_exp_f32_e32 v157, v48
	v_sub_f32_e32 v48, v61, v32
	v_add_f32_e32 v15, v83, v15
	v_exp_f32_e32 v58, v48
	v_add_f32_e32 v15, v89, v15
	v_exp_f32_e32 v62, v33
	v_sub_f32_e32 v33, v63, v32
	v_add_f32_e32 v15, v105, v15
	v_exp_f32_e32 v74, v33
	v_sub_f32_e32 v33, v34, v32
	v_add_f32_e32 v15, v157, v15
	v_exp_f32_e32 v84, v33
	v_sub_f32_e32 v33, v36, v32
	v_add_f32_e32 v15, v58, v15
	v_exp_f32_e32 v87, v33
	v_sub_f32_e32 v33, v35, v32
	v_add_f32_e32 v15, v62, v15
	v_exp_f32_e32 v94, v33
	v_sub_f32_e32 v33, v82, v32
	v_add_f32_e32 v15, v74, v15
	v_exp_f32_e32 v154, v33
	v_sub_f32_e32 v33, v37, v32
	v_add_f32_e32 v15, v84, v15
	v_exp_f32_e32 v158, v33
	v_sub_f32_e32 v33, v39, v32
	v_add_f32_e32 v15, v87, v15
	v_exp_f32_e32 v61, v33
	v_sub_f32_e32 v33, v38, v32
	v_add_f32_e32 v15, v94, v15
	v_exp_f32_e32 v73, v33
	v_sub_f32_e32 v33, v41, v32
	v_add_f32_e32 v15, v154, v15
	v_exp_f32_e32 v78, v33
	v_sub_f32_e32 v33, v40, v32
	v_add_f32_e32 v15, v158, v15
	v_exp_f32_e32 v88, v33
	v_sub_f32_e32 v33, v43, v32
	v_add_f32_e32 v15, v61, v15
	v_exp_f32_e32 v93, v33
	v_sub_f32_e32 v33, v42, v32
	v_add_f32_e32 v15, v73, v15
	v_exp_f32_e32 v153, v33
	v_sub_f32_e32 v33, v46, v32
	v_add_f32_e32 v15, v78, v15
	v_exp_f32_e32 v156, v33
	v_sub_f32_e32 v33, v44, v32
	v_add_f32_e32 v15, v88, v15
	v_exp_f32_e32 v159, v33
	v_sub_f32_e32 v33, v45, v32
	v_add_f32_e32 v15, v93, v15
	v_exp_f32_e32 v63, v33
	v_add_f32_e32 v15, v153, v15
	v_exp_f32_e32 v77, v16
	v_sub_f32_e32 v16, v18, v32
	v_add_f32_e32 v15, v156, v15
	v_exp_f32_e32 v82, v16
	v_sub_f32_e32 v16, v17, v32
	v_add_f32_e32 v15, v159, v15
	v_exp_f32_e32 v90, v16
	v_sub_f32_e32 v16, v20, v32
	v_add_f32_e32 v15, v63, v15
	v_exp_f32_e32 v92, v16
	v_sub_f32_e32 v16, v19, v32
	v_add_f32_e32 v15, v77, v15
	v_exp_f32_e32 v95, v16
	v_sub_f32_e32 v16, v22, v32
	v_add_f32_e32 v15, v82, v15
	v_exp_f32_e32 v106, v16
	v_sub_f32_e32 v16, v21, v32
	v_add_f32_e32 v15, v90, v15
	v_exp_f32_e32 v152, v16
	v_sub_f32_e32 v16, v24, v32
	v_add_f32_e32 v15, v92, v15
	v_exp_f32_e32 v51, v16
	v_sub_f32_e32 v16, v23, v32
	v_add_f32_e32 v15, v95, v15
	v_exp_f32_e32 v52, v16
	v_sub_f32_e32 v16, v26, v32
	v_add_f32_e32 v15, v106, v15
	v_exp_f32_e32 v53, v16
	v_sub_f32_e32 v16, v25, v32
	v_add_f32_e32 v15, v152, v15
	v_exp_f32_e32 v55, v16
	v_sub_f32_e32 v16, v28, v32
	v_add_f32_e32 v15, v51, v15
	v_exp_f32_e32 v56, v16
	v_sub_f32_e32 v16, v27, v32
	v_add_f32_e32 v15, v52, v15
	v_exp_f32_e32 v57, v16
	v_sub_f32_e32 v16, v30, v32
	v_add_f32_e32 v15, v53, v15
	v_exp_f32_e32 v59, v16
	v_sub_f32_e32 v16, v29, v32
	v_add_f32_e32 v15, v55, v15
	v_exp_f32_e32 v60, v16
	v_sub_f32_e32 v16, v47, v32
	v_add_f32_e32 v15, v56, v15
	v_exp_f32_e32 v43, v16
	v_sub_f32_e32 v16, v31, v32
	v_add_f32_e32 v15, v57, v15
	v_exp_f32_e32 v44, v16
	v_sub_f32_e32 v16, v161, v32
	v_add_f32_e32 v15, v59, v15
	v_exp_f32_e32 v45, v16
	v_sub_f32_e32 v16, v160, v32
	v_add_f32_e32 v15, v60, v15
	v_exp_f32_e32 v46, v16
	v_sub_f32_e32 v16, v163, v32
	v_add_f32_e32 v15, v43, v15
	v_exp_f32_e32 v47, v16
	v_sub_f32_e32 v16, v162, v32
	v_add_f32_e32 v15, v44, v15
	v_exp_f32_e32 v48, v16
	v_sub_f32_e32 v16, v165, v32
	v_add_f32_e32 v15, v45, v15
	v_exp_f32_e32 v49, v16
	v_sub_f32_e32 v16, v164, v32
	v_add_f32_e32 v15, v46, v15
	v_exp_f32_e32 v50, v16
	v_sub_f32_e32 v16, v166, v32
	v_add_f32_e32 v15, v47, v15
	v_exp_f32_e32 v35, v16
	v_sub_f32_e32 v8, v8, v32
	v_add_f32_e32 v15, v48, v15
	v_exp_f32_e32 v36, v8
	v_sub_f32_e32 v10, v10, v32
	v_add_f32_e32 v15, v49, v15
	v_exp_f32_e32 v37, v10
	v_sub_f32_e32 v9, v9, v32
	v_add_f32_e32 v15, v50, v15
	v_exp_f32_e32 v38, v9
	v_sub_f32_e32 v9, v12, v32
	v_add_f32_e32 v15, v35, v15
	v_exp_f32_e32 v39, v9
	v_sub_f32_e32 v9, v11, v32
	v_add_f32_e32 v8, v36, v15
	v_exp_f32_e32 v40, v9
	v_sub_f32_e32 v9, v14, v32
	v_add_f32_e32 v8, v37, v8
	v_exp_f32_e32 v41, v9
	v_sub_f32_e32 v9, v13, v32
	v_cvt_pk_bf16_f32 v16, v0, v1
	v_cvt_pk_bf16_f32 v17, v2, v3
	v_cvt_pk_bf16_f32 v18, v4, v5
	v_cvt_pk_bf16_f32 v19, v6, v7
	ds_read_b64_tr_b16 v[0:1], v101 offset:32768
	ds_read_b64_tr_b16 v[2:3], v101 offset:33280
	v_add_f32_e32 v8, v38, v8
	v_exp_f32_e32 v42, v9
	v_add_f32_e32 v8, v39, v8
	v_add_f32_e32 v8, v40, v8
	v_add_f32_e32 v8, v41, v8
	v_add_f32_e32 v33, v42, v8
	s_waitcnt lgkmcnt(0)
; #define LAS __attribute__((address_space(3)))
; __device__ __forceinline__ float sum_x32(float v) { const unsigned u = __builtin_bit_cast(unsigned, v); auto rr = __builtin_amdgcn_permlane32_swap(u, u, false, false); return __builtin_bit_cast(float, (unsigned)rr[0]) + __builtin_bit_cast(float, (unsigned)rr[1]); }
; __device__ __forceinline__ unsigned cvt_pk_bf16(float lo, float hi) { unsigned r; asm volatile("v_cvt_pk_bf16_f32 %0, %1, %2" : "=v"(r) : "v"(lo), "v"(hi)); return r; }
; __device__ __forceinline__ s16x4 vtr(const LAS unsigned char* p) { return __builtin_bit_cast(s16x4, __builtin_amdgcn_ds_read_tr16_b64_v4i16((LAS s16x4*)p)); }
; __device__ __forceinline__ void attn_phase(LAS unsigned char* lds, const bf16* U, bf16* YA, const float* sinks, const float* rel_bias, int G, int c, int wbase, int y8) {
;     ...
;             l = sum_x32(l); l += __builtin_amdgcn_exp2f(sink2 - mx);
;             f32x16 o[2]; o[0] = (f32x16){}; o[1] = (f32x16){};
;             const LAS unsigned char* vb = lds + VIMG + ((lane >> 4) & 1) * 32 + (lane & 3) * 8 + (4 * hi + ((lane & 15) >> 2)) * 64;
; #pragma unroll
;             for (int jt = 0; jt < 5; ++jt)
; #pragma unroll
;                 for (int s = 0; s < 2; ++s) { u32x4 w; w.x = cvt_pk_bf16(p[jt][8 * s], p[jt][8 * s + 1]); w.y = cvt_pk_bf16(p[jt][8 * s + 2], p[jt][8 * s + 3]); w.z = cvt_pk_bf16(p[jt][8 * s + 4], p[jt][8 * s + 5]); w.w = cvt_pk_bf16(p[jt][8 * s + 6], p[jt][8 * s + 7]);
;                     const bf16x8 pa = __builtin_bit_cast(bf16x8, w);
; #pragma unroll
;                     for (int d0 = 0; d0 < 2; ++d0) { const LAS unsigned char* vp = vb + d0 * 16384 + (32 * (kt0 + jt) + 16 * s) * 64; const s16x4 lo = vtr(vp), hv = vtr(vp + 8 * 64);
;                         const bf16x8 vf = (bf16x8){lo[0], lo[1], lo[2], lo[3], hv[0], hv[1], hv[2], hv[3]};
;                         o[d0] = __builtin_amdgcn_mfma_f32_32x32x16_bf16(pa, vf, o[d0], 0, 0, 0); } }
;             if (hi == 0) lscr[r32] = l;
	v_mfma_f32_32x32x16_bf16 v[0:15], v[16:19], v[0:3], 0
	ds_read_b64_tr_b16 v[20:21], v101 offset:49152
	ds_read_b64_tr_b16 v[22:23], v101 offset:49664
	v_cvt_pk_bf16_f32 v160, v64, v66
	v_cvt_pk_bf16_f32 v161, v68, v72
	v_cvt_pk_bf16_f32 v162, v75, v81
	v_cvt_pk_bf16_f32 v163, v86, v107
	ds_read_b64_tr_b16 v[164:165], v101 offset:33792
	ds_read_b64_tr_b16 v[166:167], v101 offset:34304
	v_mov_b32_e32 v34, v33
	s_waitcnt lgkmcnt(2)
	v_mfma_f32_32x32x16_bf16 v[16:31], v[16:19], v[20:23], 0
	v_permlane32_swap_b32_e32 v33, v34
	s_waitcnt lgkmcnt(0)
	v_mfma_f32_32x32x16_bf16 v[0:15], v[160:163], v[164:167], v[0:15]
	ds_read_b64_tr_b16 v[164:165], v101 offset:50176
	ds_read_b64_tr_b16 v[166:167], v101 offset:50688
	v_cvt_pk_bf16_f32 v64, v65, v67
	v_cvt_pk_bf16_f32 v65, v70, v76
	v_cvt_pk_bf16_f32 v66, v80, v85
	v_cvt_pk_bf16_f32 v67, v91, v155
	s_waitcnt lgkmcnt(0)
	v_mfma_f32_32x32x16_bf16 v[16:31], v[160:163], v[164:167], v[16:31]
	ds_read_b64_tr_b16 v[160:161], v102 offset:32768
	ds_read_b64_tr_b16 v[162:163], v102 offset:33280
	s_waitcnt lgkmcnt(0)
	v_mfma_f32_32x32x16_bf16 v[0:15], v[64:67], v[160:163], v[0:15]
	ds_read_b64_tr_b16 v[160:161], v102 offset:49152
	ds_read_b64_tr_b16 v[162:163], v102 offset:49664
	s_waitcnt lgkmcnt(0)
	v_mfma_f32_32x32x16_bf16 v[16:31], v[64:67], v[160:163], v[16:31]
	v_cvt_pk_bf16_f32 v64, v54, v69
	v_cvt_pk_bf16_f32 v65, v71, v79
	v_cvt_pk_bf16_f32 v66, v83, v89
	v_cvt_pk_bf16_f32 v67, v105, v157
	ds_read_b64_tr_b16 v[68:69], v102 offset:33792
	ds_read_b64_tr_b16 v[70:71], v102 offset:34304
	s_waitcnt lgkmcnt(0)
	v_mfma_f32_32x32x16_bf16 v[0:15], v[64:67], v[68:71], v[0:15]
	ds_read_b64_tr_b16 v[68:69], v102 offset:50176
	ds_read_b64_tr_b16 v[70:71], v102 offset:50688
	s_waitcnt lgkmcnt(0)
	v_mfma_f32_32x32x16_bf16 v[16:31], v[64:67], v[68:71], v[16:31]
	v_cvt_pk_bf16_f32 v64, v58, v62
	v_cvt_pk_bf16_f32 v65, v74, v84
	v_cvt_pk_bf16_f32 v66, v87, v94
	v_cvt_pk_bf16_f32 v67, v154, v158
	ds_read_b64_tr_b16 v[68:69], v103 offset:32768
	ds_read_b64_tr_b16 v[70:71], v103 offset:33280
	s_waitcnt lgkmcnt(0)
	v_mfma_f32_32x32x16_bf16 v[0:15], v[64:67], v[68:71], v[0:15]
	ds_read_b64_tr_b16 v[68:69], v103 offset:49152
	ds_read_b64_tr_b16 v[70:71], v103 offset:49664
	s_waitcnt lgkmcnt(0)
	v_mfma_f32_32x32x16_bf16 v[16:31], v[64:67], v[68:71], v[16:31]
	v_cvt_pk_bf16_f32 v64, v61, v73
	v_cvt_pk_bf16_f32 v65, v78, v88
	v_cvt_pk_bf16_f32 v66, v93, v153
	v_cvt_pk_bf16_f32 v67, v156, v159
	ds_read_b64_tr_b16 v[68:69], v103 offset:33792
	ds_read_b64_tr_b16 v[70:71], v103 offset:34304
	s_waitcnt lgkmcnt(0)
	v_mfma_f32_32x32x16_bf16 v[0:15], v[64:67], v[68:71], v[0:15]
	ds_read_b64_tr_b16 v[68:69], v103 offset:50176
	ds_read_b64_tr_b16 v[70:71], v103 offset:50688
	v_cvt_pk_bf16_f32 v62, v63, v77
	v_cvt_pk_bf16_f32 v63, v82, v90
	s_waitcnt lgkmcnt(0)
	v_mfma_f32_32x32x16_bf16 v[16:31], v[64:67], v[68:71], v[16:31]
	v_cvt_pk_bf16_f32 v64, v92, v95
	v_cvt_pk_bf16_f32 v65, v106, v152
	ds_read_b64_tr_b16 v[66:67], v104 offset:32768
	ds_read_b64_tr_b16 v[68:69], v104 offset:33280
	s_waitcnt lgkmcnt(0)
	v_mfma_f32_32x32x16_bf16 v[0:15], v[62:65], v[66:69], v[0:15]
	ds_read_b64_tr_b16 v[66:67], v104 offset:49152
	ds_read_b64_tr_b16 v[68:69], v104 offset:49664
	v_cvt_pk_bf16_f32 v52, v51, v52
	v_cvt_pk_bf16_f32 v53, v53, v55
	v_cvt_pk_bf16_f32 v54, v56, v57
	v_cvt_pk_bf16_f32 v55, v59, v60
	ds_read_b64_tr_b16 v[56:57], v104 offset:33792
	ds_read_b64_tr_b16 v[58:59], v104 offset:34304
	s_waitcnt lgkmcnt(2)
	v_mfma_f32_32x32x16_bf16 v[16:31], v[62:65], v[66:69], v[16:31]
	s_waitcnt lgkmcnt(0)
	v_mfma_f32_32x32x16_bf16 v[0:15], v[52:55], v[56:59], v[0:15]
	ds_read_b64_tr_b16 v[56:57], v104 offset:50176
	ds_read_b64_tr_b16 v[58:59], v104 offset:50688
	v_cvt_pk_bf16_f32 v44, v43, v44
	v_cvt_pk_bf16_f32 v45, v45, v46
	v_cvt_pk_bf16_f32 v46, v47, v48
	v_cvt_pk_bf16_f32 v47, v49, v50
	s_waitcnt lgkmcnt(0)
	v_mfma_f32_32x32x16_bf16 v[16:31], v[52:55], v[56:59], v[16:31]
	v_add_u32_e32 v52, s79, v125
	ds_read_b64_tr_b16 v[48:49], v52 offset:32768
	ds_read_b64_tr_b16 v[50:51], v52 offset:33280
	s_waitcnt lgkmcnt(0)
	v_mfma_f32_32x32x16_bf16 v[0:15], v[44:47], v[48:51], v[0:15]
	ds_read_b64_tr_b16 v[48:49], v52 offset:49152
	ds_read_b64_tr_b16 v[50:51], v52 offset:49664
	v_cvt_pk_bf16_f32 v36, v35, v36
	v_cvt_pk_bf16_f32 v37, v37, v38
	v_cvt_pk_bf16_f32 v38, v39, v40
	v_cvt_pk_bf16_f32 v39, v41, v42
	ds_read_b64_tr_b16 v[40:41], v52 offset:33792
	ds_read_b64_tr_b16 v[42:43], v52 offset:34304
	s_waitcnt lgkmcnt(2)
	v_mfma_f32_32x32x16_bf16 v[16:31], v[44:47], v[48:51], v[16:31]
	s_waitcnt lgkmcnt(0)
	v_mfma_f32_32x32x16_bf16 v[0:15], v[36:39], v[40:43], v[0:15]
	ds_read_b64_tr_b16 v[40:41], v52 offset:50176
	ds_read_b64_tr_b16 v[42:43], v52 offset:50688
	s_waitcnt lgkmcnt(0)
	v_mfma_f32_32x32x16_bf16 v[16:31], v[36:39], v[40:43], v[16:31]
	s_and_saveexec_b64 s[4:5], s[2:3]
	s_cbranch_execz .LBB0_570
	v_sub_f32_e32 v32, v151, v32
	v_exp_f32_e32 v32, v32
	v_add_f32_e32 v33, v33, v34
	v_add_f32_e32 v32, v33, v32
	ds_write_b32 v126, v32

; __device__ __forceinline__ float fast_exp(float x) { return __builtin_amdgcn_exp2f(x * LOG2E); }
; #define LRU_LOAD_RAW(st_) do { const int t_ = ck * TC + (st_) * 32 + r32; const size_t m_ = (size_t)b * SEQ + t_; _Pragma("unroll") for (int ks = 0; ks < 4; ++ks) _Pragma("unroll") for (int j = 0; j < 4; ++j) { \
;             const int back_ = 3 - j; const size_t mm_ = (t_ >= back_) ? m_ - back_ : m_; raw[ks][j] = *(const u32x4*)(U + mm_ * NIN + C_LX + ch0 + 16 * ks + 8 * hi); } } while (0)
; __device__ __forceinline__ void lru_scan(LAS unsigned char* lds, const bf16* U, bf16* HR, bf16* PQ, float* AGG, const bf16* Wt, const float* conv_w, const float* conv_b,
;                                          const float* b_rg, const float* b_ig, const float* lam, int G, int c, int wbase) {
;     ...
;         for (int j = 0; j < 4; ++j) cw[j * 64 + lane] = conv_w[j * DM + ch0 + lane];
;         cw[4 * 64 + lane] = conv_b[ch0 + lane];
;         float brg[2], big[2], sp8[2], carry[2], prodA[2];
; #pragma unroll
;         for (int ct = 0; ct < 2; ++ct) { const int ch = ch0 + 32 * ct + r32; brg[ct] = b_rg[ch] * -LOG2E; big[ct] = b_ig[ch] * -LOG2E; { const float x = fast_exp(-lam[ch]); sp8[ct] = (-8.f * LOG2E) * (x < 0.25f ? x * (1.f - x * (0.5f - x * ((1.f / 3.f) - x * (0.25f - x * (0.2f - x * (1.f / 6.f)))))) : (__builtin_amdgcn_logf(1.f + x) * 0.6931471805599453f)); } carry[ct] = 0.f; prodA[ct] = 1.f; }
;         asm volatile("s_waitcnt lgkmcnt(0)" ::: "memory");
;         u32x4 raw[4][4];
;     ...
;         LRU_LOAD_RAW(0);
.LBB0_595:
	v_or_b32_e32 v0, s30, v145
	v_lshlrev_b32_e32 v232, 2, v0
	v_lshl_add_u64 v[0:1], s[18:19], 0, v[232:233]
	v_add_co_u32_e32 v2, vcc, 0x1000, v0
	global_load_dword v4, v232, s[18:19]
	s_nop 0
	v_addc_co_u32_e32 v3, vcc, 0, v1, vcc
	global_load_dword v2, v[2:3], off
	s_waitcnt vmcnt(0)
	ds_write2st64_b32 v151, v4, v2 offset0:32 offset1:33
	v_add_co_u32_e32 v2, vcc, 0x2000, v0
	s_nop 1
	v_addc_co_u32_e32 v3, vcc, 0, v1, vcc
	v_add_co_u32_e32 v0, vcc, 0x3000, v0
	global_load_dword v2, v[2:3], off
	s_nop 0
	v_addc_co_u32_e32 v1, vcc, 0, v1, vcc
	global_load_dword v0, v[0:1], off
	s_waitcnt vmcnt(0)
	ds_write2st64_b32 v151, v2, v0 offset0:34 offset1:35
	global_load_dword v0, v232, s[20:21]
	s_waitcnt vmcnt(0)
	ds_write_b32 v151, v0 offset:9216
	v_or_b32_e32 v0, s30, v144
	v_lshlrev_b32_e32 v232, 2, v0
	global_load_dword v0, v232, s[22:23]
	global_load_dword v1, v232, s[24:25]
	global_load_dword v2, v232, s[26:27]
	s_waitcnt vmcnt(0)
	v_mul_f32_e32 v2, 0xbfb8aa3b, v2
	v_exp_f32_e32 v3, v2
	s_nop 0
	v_cmp_ngt_f32_e32 vcc, s82, v3
	s_and_saveexec_b64 s[4:5], vcc
	s_xor_b64 s[4:5], exec, s[4:5]
	v_add_f32_e32 v2, 1.0, v3
	v_log_f32_e32 v2, v2
	s_nop 0
	v_mul_f32_e32 v2, 0x3f317218, v2
	s_andn2_saveexec_b64 s[4:5], s[4:5]
	v_mov_b32_e32 v2, 0x3e4ccccd
	v_fmamk_f32 v2, v3, 0xbe2aaaab, v2
	v_fma_f32 v2, -v3, v2, s82
	s_mov_b32 s6, 0x3eaaaaab
	v_fma_f32 v2, -v3, v2, s6
	v_fma_f32 v2, -v3, v2, 0.5
	v_fma_f32 v2, -v3, v2, 1.0
	v_mul_f32_e32 v2, v3, v2
	s_or_b64 exec, exec, s[4:5]
	v_lshl_add_u64 v[4:5], s[26:27], 0, v[232:233]
	global_load_dword v3, v[4:5], off offset:128
	v_lshl_add_u64 v[4:5], s[22:23], 0, v[232:233]
	v_lshl_add_u64 v[6:7], s[24:25], 0, v[232:233]
	global_load_dword v4, v[4:5], off offset:128
	s_nop 0
	global_load_dword v5, v[6:7], off offset:128
	s_waitcnt vmcnt(2)
	v_mul_f32_e32 v3, 0xbfb8aa3b, v3
	v_exp_f32_e32 v6, v3
	s_nop 0
	v_cmp_ngt_f32_e32 vcc, s82, v6
	s_and_saveexec_b64 s[4:5], vcc
	s_xor_b64 s[4:5], exec, s[4:5]
	v_add_f32_e32 v3, 1.0, v6
	v_log_f32_e32 v3, v3
	s_nop 0
	v_mul_f32_e32 v3, 0x3f317218, v3
	s_andn2_saveexec_b64 s[4:5], s[4:5]
	v_mov_b32_e32 v3, 0x3e4ccccd
	v_fmamk_f32 v3, v6, 0xbe2aaaab, v3
	v_fma_f32 v3, -v6, v3, s82
	s_mov_b32 s6, 0x3eaaaaab
	v_fma_f32 v3, -v6, v3, s6
	v_fma_f32 v3, -v6, v3, 0.5
	v_fma_f32 v3, -v6, v3, 1.0
	v_mul_f32_e32 v3, v6, v3
	s_or_b64 exec, exec, s[4:5]
	s_and_b32 s33, s1, 31
	s_ashr_i32 s28, s1, 9
	v_lshl_or_b32 v16, s33, 7, v144
	s_ashr_i32 s29, s28, 31
	s_lshl_b64 s[4:5], s[28:29], 12
	v_cmp_gt_u32_e32 vcc, 3, v16
	v_or_b32_e32 v6, s4, v16
	v_mov_b32_e32 v7, s5
	v_cndmask_b32_e64 v9, -1, 0, vcc
	v_cndmask_b32_e64 v8, -3, 0, vcc
	v_lshl_add_u64 v[8:9], v[8:9], 0, v[6:7]
	v_mov_b64_e32 v[10:11], s[14:15]
	v_mad_u64_u32 v[12:13], s[6:7], v8, s87, v[10:11]
	v_mad_i32_i24 v13, v9, s87, v13
	s_lshl_b32 s6, s30, 1
	s_mov_b32 s7, s40
	v_cmp_gt_u32_e32 vcc, 2, v16
	v_lshl_add_u64 v[8:9], v[12:13], 0, s[6:7]
	v_mov_b32_e32 v153, v233
	v_cndmask_b32_e64 v13, -1, 0, vcc
	v_cndmask_b32_e64 v12, -2, 0, vcc
	v_lshl_add_u64 v[12:13], v[12:13], 0, v[6:7]
	v_mad_u64_u32 v[14:15], s[10:11], v12, s87, v[10:11]
	v_mad_i32_i24 v15, v13, s87, v15
	v_cmp_ne_u32_e32 vcc, 0, v16
	v_lshl_add_u64 v[12:13], v[14:15], 0, s[6:7]
	s_waitcnt lgkmcnt(0)
	v_lshl_add_u64 v[8:9], v[8:9], 0, v[152:153]
	v_cndmask_b32_e64 v14, 0, 1, vcc
	v_sub_co_u32_e32 v14, vcc, v6, v14
	v_mad_u64_u32 v[14:15], s[10:11], v14, s87, v[10:11]
	s_nop 0
	v_subbrev_co_u32_e32 v7, vcc, 0, v7, vcc
	v_mad_i32_i24 v15, v7, s87, v15
	v_mad_u64_u32 v[6:7], s[10:11], v6, s87, v[10:11]
	v_mov_b32_e32 v10, 0x2c00
	v_mad_i32_i24 v7, s5, v10, v7
	v_lshl_add_u64 v[14:15], v[14:15], 0, s[6:7]
	v_lshl_add_u64 v[6:7], v[6:7], 0, s[6:7]
	v_lshl_add_u64 v[12:13], v[12:13], 0, v[152:153]
	v_lshl_add_u64 v[14:15], v[14:15], 0, v[152:153]
	v_lshl_add_u64 v[6:7], v[6:7], 0, v[152:153]
	global_load_dwordx4 v[60:63], v[8:9], off offset:3072
	global_load_dwordx4 v[64:67], v[8:9], off offset:3104
	global_load_dwordx4 v[68:71], v[12:13], off offset:3072
	global_load_dwordx4 v[72:75], v[12:13], off offset:3104
	global_load_dwordx4 v[76:79], v[14:15], off offset:3072
	global_load_dwordx4 v[80:83], v[14:15], off offset:3104
	global_load_dwordx4 v[84:87], v[6:7], off offset:3072
	global_load_dwordx4 v[88:91], v[6:7], off offset:3104
	global_load_dwordx4 v[92:95], v[8:9], off offset:3136
	global_load_dwordx4 v[96:99], v[8:9], off offset:3168
	global_load_dwordx4 v[100:103], v[12:13], off offset:3136
	global_load_dwordx4 v[104:107], v[12:13], off offset:3168
	global_load_dwordx4 v[108:111], v[14:15], off offset:3136
	global_load_dwordx4 v[112:115], v[14:15], off offset:3168
	global_load_dwordx4 v[116:119], v[6:7], off offset:3136
	global_load_dwordx4 v[120:123], v[6:7], off offset:3168
	s_and_b32 s5, s13, 31
	s_lshl_b32 s6, s5, 7
	v_mul_f32_e32 v203, 0xbfb8aa3b, v0
	v_or_b32_e32 v0, s6, v182
	s_lshr_b32 s4, s1, 5
	v_mul_f32_e32 v153, 0xc138aa3b, v2
	v_lshlrev_b32_e32 v2, 10, v0
	v_or_b32_e32 v0, s6, v196
	s_waitcnt vmcnt(16)
	v_mul_f32_e32 v202, 0xbfb8aa3b, v5
	s_and_b32 s7, s4, 15
	v_lshlrev_b32_e32 v5, 10, v0
	v_or_b32_e32 v0, s6, v194
	v_mul_f32_e32 v192, 0xbfb8aa3b, v4
	v_or_b32_e32 v205, s6, v144
	s_lshl_b32 s4, s7, 7
	v_lshl_or_b32 v4, s7, 6, v183
	v_lshlrev_b32_e32 v6, 10, v0
	v_or_b32_e32 v0, s6, v190
	s_mul_hi_i32 s6, s28, 0x2c00000
	s_mul_i32 s7, s28, 0x2c00000
	v_mul_f32_e32 v204, 0xbfb8aa3b, v1
	v_lshlrev_b32_e32 v7, 10, v0
	v_mov_b32_e32 v1, s6
	v_or_b32_e32 v0, s7, v150
	s_mov_b32 s5, s40
	v_mad_u64_u32 v[0:1], s[6:7], v205, s87, v[0:1]
	v_lshl_add_u64 v[154:155], v[0:1], 0, s[4:5]
	s_lshl_b64 s[4:5], s[28:29], 22
	v_or3_b32 v0, s4, v2, v4
	v_mov_b32_e32 v1, s5
	v_lshlrev_b64 v[156:157], 1, v[0:1]
	v_or3_b32 v0, s4, v5, v4
	v_lshlrev_b64 v[158:159], 1, v[0:1]
	v_or3_b32 v0, s4, v6, v4
	v_lshlrev_b64 v[160:161], 1, v[0:1]
	v_or3_b32 v0, s4, v7, v4
	v_mul_f32_e32 v206, 0xc138aa3b, v3
	s_mov_b32 s34, 0
	v_lshlrev_b64 v[162:163], 1, v[0:1]
	v_mov_b32_e32 v171, 0
	v_mov_b32_e32 v168, 1.0
	v_mov_b32_e32 v164, 1.0
	v_mov_b32_e32 v167, 0
	s_waitcnt vmcnt(0)
	s_branch .LBB0_605

; #define LAS __attribute__((address_space(3)))
; __device__ __forceinline__ u32x4 pack8(const f32x4 a, const f32x4 b) { u32x4 w; w.x = cvt_pk_bf16(a[0], a[1]); w.y = cvt_pk_bf16(a[2], a[3]); w.z = cvt_pk_bf16(b[0], b[1]); w.w = cvt_pk_bf16(b[2], b[3]); return w; }
; __device__ __forceinline__ void lru_scan(LAS unsigned char* lds, const bf16* U, bf16* HR, bf16* PQ, float* AGG, const bf16* Wt, const float* conv_w, const float* conv_b,
;                                          const float* b_rg, const float* b_ig, const float* lam, int G, int c, int wbase) {
;     ...
;         for (int st = 0; st < 4; ++st) {
;             const int t0 = ck * TC + st * 32, t = t0 + r32;
;             bf16x8 af[4];
; #pragma unroll
;             for (int ks = 0; ks < 4; ++ks) { const int cl = 16 * ks + 8 * hi; f32x4 x0 = *(const LAS f32x4*)(cw + 256 + cl), x1 = *(const LAS f32x4*)(cw + 256 + cl + 4);
; #pragma unroll
;                 for (int j = 0; j < 4; ++j) { const int back = 3 - j; const bool ok = t >= back;
;                     f32x4 v0, v1; pg8::unpack8(raw[ks][j], v0, v1);
;                     const f32x4 w0 = *(const LAS f32x4*)(cw + j * 64 + cl), w1 = *(const LAS f32x4*)(cw + j * 64 + cl + 4);
;                     if (ok) { x0 = x0 + w0 * v0; x1 = x1 + w1 * v1; } }
;                 af[ks] = __builtin_bit_cast(bf16x8, pg8::pack8(x0, x1)); }
.LBB0_605:
	ds_read_b128 v[0:3], v186 offset:9216
	ds_read_b128 v[4:7], v186 offset:9232
	v_add_u32_e32 v8, s34, v205
	v_cmp_lt_u32_e32 vcc, 2, v8
	s_and_saveexec_b64 s[4:5], vcc
	s_cbranch_execz .LBB0_623
	ds_read_b128 v[10:13], v186 offset:8192
	ds_read_b128 v[14:17], v186 offset:8208
	s_waitcnt vmcnt(23)
	v_lshlrev_b32_e32 v18, 16, v62
	v_and_b32_e32 v19, 0xffff0000, v62
	v_lshlrev_b32_e32 v20, 16, v63
	v_and_b32_e32 v21, 0xffff0000, v63
	v_lshlrev_b32_e32 v22, 16, v60
	v_and_b32_e32 v23, 0xffff0000, v60
	v_lshlrev_b32_e32 v24, 16, v61
	v_and_b32_e32 v25, 0xffff0000, v61
	s_waitcnt lgkmcnt(1)
	v_pk_fma_f32 v[2:3], v[12:13], v[24:25], v[2:3]
	v_pk_fma_f32 v[0:1], v[10:11], v[22:23], v[0:1]
	s_waitcnt lgkmcnt(0)
	v_pk_fma_f32 v[6:7], v[16:17], v[20:21], v[6:7]
	v_pk_fma_f32 v[4:5], v[14:15], v[18:19], v[4:5]
	s_or_b64 exec, exec, s[4:5]
	v_cmp_lt_u32_e64 s[4:5], 1, v8
	s_and_saveexec_b64 s[6:7], s[4:5]
	s_cbranch_execnz .LBB0_624

; #define LAS __attribute__((address_space(3)))
; __device__ __forceinline__ u32x4 pack8(const f32x4 a, const f32x4 b) { u32x4 w; w.x = cvt_pk_bf16(a[0], a[1]); w.y = cvt_pk_bf16(a[2], a[3]); w.z = cvt_pk_bf16(b[0], b[1]); w.w = cvt_pk_bf16(b[2], b[3]); return w; }
; __device__ __forceinline__ void lru_scan(LAS unsigned char* lds, const bf16* U, bf16* HR, bf16* PQ, float* AGG, const bf16* Wt, const float* conv_w, const float* conv_b,
;                                          const float* b_rg, const float* b_ig, const float* lam, int G, int c, int wbase) {
;     ...
;             for (int ks = 0; ks < 4; ++ks) { const int cl = 16 * ks + 8 * hi; f32x4 x0 = *(const LAS f32x4*)(cw + 256 + cl), x1 = *(const LAS f32x4*)(cw + 256 + cl + 4);
; #pragma unroll
;                 for (int j = 0; j < 4; ++j) { const int back = 3 - j; const bool ok = t >= back;
;                     f32x4 v0, v1; pg8::unpack8(raw[ks][j], v0, v1);
;                     const f32x4 w0 = *(const LAS f32x4*)(cw + j * 64 + cl), w1 = *(const LAS f32x4*)(cw + j * 64 + cl + 4);
;                     if (ok) { x0 = x0 + w0 * v0; x1 = x1 + w1 * v1; } }
;                 af[ks] = __builtin_bit_cast(bf16x8, pg8::pack8(x0, x1)); }
.LBB0_608:
	ds_read_b128 v[8:11], v186 offset:8704
	ds_read_b128 v[12:15], v186 offset:8720
	s_waitcnt vmcnt(19)
	v_lshlrev_b32_e32 v16, 16, v78
	v_and_b32_e32 v17, 0xffff0000, v78
	v_lshlrev_b32_e32 v18, 16, v79
	v_and_b32_e32 v19, 0xffff0000, v79
	v_lshlrev_b32_e32 v20, 16, v76
	v_and_b32_e32 v21, 0xffff0000, v76
	v_lshlrev_b32_e32 v22, 16, v77
	v_and_b32_e32 v23, 0xffff0000, v77
	s_waitcnt lgkmcnt(1)
	v_pk_fma_f32 v[2:3], v[10:11], v[22:23], v[2:3]
	v_pk_fma_f32 v[0:1], v[8:9], v[20:21], v[0:1]
	s_waitcnt lgkmcnt(0)
	v_pk_fma_f32 v[6:7], v[14:15], v[18:19], v[6:7]
	v_pk_fma_f32 v[4:5], v[12:13], v[16:17], v[4:5]
.LBB0_609:
	s_or_b64 exec, exec, s[10:11]
	ds_read_b128 v[8:11], v186 offset:8960
	ds_read_b128 v[12:15], v186 offset:8976
	s_waitcnt vmcnt(17)
	v_lshlrev_b32_e32 v16, 16, v86
	v_and_b32_e32 v17, 0xffff0000, v86
	v_lshlrev_b32_e32 v18, 16, v87
	v_and_b32_e32 v19, 0xffff0000, v87
	s_waitcnt lgkmcnt(0)
	v_pk_fma_f32 v[6:7], v[14:15], v[18:19], v[6:7]
	v_pk_fma_f32 v[4:5], v[12:13], v[16:17], v[4:5]
	v_lshlrev_b32_e32 v12, 16, v84
	v_and_b32_e32 v13, 0xffff0000, v84
	v_lshlrev_b32_e32 v14, 16, v85
	v_and_b32_e32 v15, 0xffff0000, v85
	v_pk_fma_f32 v[2:3], v[10:11], v[14:15], v[2:3]
	v_pk_fma_f32 v[0:1], v[8:9], v[12:13], v[0:1]
	s_nop 0
	v_cvt_pk_bf16_f32 v124, v0, v1
	v_cvt_pk_bf16_f32 v125, v2, v3
	v_cvt_pk_bf16_f32 v126, v4, v5
	v_cvt_pk_bf16_f32 v127, v6, v7
	ds_read_b128 v[0:3], v186 offset:9280
	ds_read_b128 v[4:7], v186 offset:9296
	s_and_saveexec_b64 s[10:11], vcc
	s_cbranch_execz .LBB0_625
	ds_read_b128 v[8:11], v186 offset:8256
	ds_read_b128 v[12:15], v186 offset:8272
	v_lshlrev_b32_e32 v16, 16, v66
	v_and_b32_e32 v17, 0xffff0000, v66
	v_lshlrev_b32_e32 v18, 16, v67
	v_and_b32_e32 v19, 0xffff0000, v67
	v_lshlrev_b32_e32 v20, 16, v64
	v_and_b32_e32 v21, 0xffff0000, v64
	v_lshlrev_b32_e32 v22, 16, v65
	v_and_b32_e32 v23, 0xffff0000, v65
	s_waitcnt lgkmcnt(1)
	v_pk_fma_f32 v[2:3], v[10:11], v[22:23], v[2:3]
	v_pk_fma_f32 v[0:1], v[8:9], v[20:21], v[0:1]
	s_waitcnt lgkmcnt(0)
	v_pk_fma_f32 v[6:7], v[14:15], v[18:19], v[6:7]
	v_pk_fma_f32 v[4:5], v[12:13], v[16:17], v[4:5]
	s_or_b64 exec, exec, s[10:11]
	s_and_saveexec_b64 s[10:11], s[4:5]
	s_cbranch_execnz .LBB0_626

; #define LAS __attribute__((address_space(3)))
; __device__ __forceinline__ u32x4 pack8(const f32x4 a, const f32x4 b) { u32x4 w; w.x = cvt_pk_bf16(a[0], a[1]); w.y = cvt_pk_bf16(a[2], a[3]); w.z = cvt_pk_bf16(b[0], b[1]); w.w = cvt_pk_bf16(b[2], b[3]); return w; }
; __device__ __forceinline__ void lru_scan(LAS unsigned char* lds, const bf16* U, bf16* HR, bf16* PQ, float* AGG, const bf16* Wt, const float* conv_w, const float* conv_b,
;                                          const float* b_rg, const float* b_ig, const float* lam, int G, int c, int wbase) {
;     ...
;             for (int ks = 0; ks < 4; ++ks) { const int cl = 16 * ks + 8 * hi; f32x4 x0 = *(const LAS f32x4*)(cw + 256 + cl), x1 = *(const LAS f32x4*)(cw + 256 + cl + 4);
; #pragma unroll
;                 for (int j = 0; j < 4; ++j) { const int back = 3 - j; const bool ok = t >= back;
;                     f32x4 v0, v1; pg8::unpack8(raw[ks][j], v0, v1);
;                     const f32x4 w0 = *(const LAS f32x4*)(cw + j * 64 + cl), w1 = *(const LAS f32x4*)(cw + j * 64 + cl + 4);
;                     if (ok) { x0 = x0 + w0 * v0; x1 = x1 + w1 * v1; } }
;                 af[ks] = __builtin_bit_cast(bf16x8, pg8::pack8(x0, x1)); }
.LBB0_613:
	s_or_b64 exec, exec, s[10:11]
	ds_read_b128 v[8:11], v186 offset:9024
	ds_read_b128 v[12:15], v186 offset:9040
	s_waitcnt vmcnt(16)
	v_lshlrev_b32_e32 v16, 16, v90
	v_and_b32_e32 v17, 0xffff0000, v90
	v_lshlrev_b32_e32 v18, 16, v91
	v_and_b32_e32 v19, 0xffff0000, v91
	s_waitcnt lgkmcnt(0)
	v_pk_fma_f32 v[6:7], v[14:15], v[18:19], v[6:7]
	v_pk_fma_f32 v[4:5], v[12:13], v[16:17], v[4:5]
	v_lshlrev_b32_e32 v12, 16, v88
	v_and_b32_e32 v13, 0xffff0000, v88
	v_lshlrev_b32_e32 v14, 16, v89
	v_and_b32_e32 v15, 0xffff0000, v89
	v_pk_fma_f32 v[2:3], v[10:11], v[14:15], v[2:3]
	v_pk_fma_f32 v[0:1], v[8:9], v[12:13], v[0:1]
	s_nop 0
	v_cvt_pk_bf16_f32 v128, v0, v1
	v_cvt_pk_bf16_f32 v129, v2, v3
	v_cvt_pk_bf16_f32 v130, v4, v5
	v_cvt_pk_bf16_f32 v131, v6, v7
	ds_read_b128 v[0:3], v186 offset:9344
	ds_read_b128 v[4:7], v186 offset:9360
	s_and_saveexec_b64 s[10:11], vcc
	s_cbranch_execz .LBB0_627
	ds_read_b128 v[8:11], v186 offset:8320
	ds_read_b128 v[12:15], v186 offset:8336
	s_waitcnt vmcnt(15)
	v_lshlrev_b32_e32 v16, 16, v94
	v_and_b32_e32 v17, 0xffff0000, v94
	v_lshlrev_b32_e32 v18, 16, v95
	v_and_b32_e32 v19, 0xffff0000, v95
	v_lshlrev_b32_e32 v20, 16, v92
	v_and_b32_e32 v21, 0xffff0000, v92
	v_lshlrev_b32_e32 v22, 16, v93
	v_and_b32_e32 v23, 0xffff0000, v93
	s_waitcnt lgkmcnt(1)
	v_pk_fma_f32 v[2:3], v[10:11], v[22:23], v[2:3]
	v_pk_fma_f32 v[0:1], v[8:9], v[20:21], v[0:1]
	s_waitcnt lgkmcnt(0)
	v_pk_fma_f32 v[6:7], v[14:15], v[18:19], v[6:7]
	v_pk_fma_f32 v[4:5], v[12:13], v[16:17], v[4:5]
	s_or_b64 exec, exec, s[10:11]
	s_and_saveexec_b64 s[10:11], s[4:5]
	s_cbranch_execnz .LBB0_628

; #define LAS __attribute__((address_space(3)))
; __device__ __forceinline__ u32x4 pack8(const f32x4 a, const f32x4 b) { u32x4 w; w.x = cvt_pk_bf16(a[0], a[1]); w.y = cvt_pk_bf16(a[2], a[3]); w.z = cvt_pk_bf16(b[0], b[1]); w.w = cvt_pk_bf16(b[2], b[3]); return w; }
; __device__ __forceinline__ void lru_scan(LAS unsigned char* lds, const bf16* U, bf16* HR, bf16* PQ, float* AGG, const bf16* Wt, const float* conv_w, const float* conv_b,
;                                          const float* b_rg, const float* b_ig, const float* lam, int G, int c, int wbase) {
;     ...
;             for (int ks = 0; ks < 4; ++ks) { const int cl = 16 * ks + 8 * hi; f32x4 x0 = *(const LAS f32x4*)(cw + 256 + cl), x1 = *(const LAS f32x4*)(cw + 256 + cl + 4);
; #pragma unroll
;                 for (int j = 0; j < 4; ++j) { const int back = 3 - j; const bool ok = t >= back;
;                     f32x4 v0, v1; pg8::unpack8(raw[ks][j], v0, v1);
;                     const f32x4 w0 = *(const LAS f32x4*)(cw + j * 64 + cl), w1 = *(const LAS f32x4*)(cw + j * 64 + cl + 4);
;                     if (ok) { x0 = x0 + w0 * v0; x1 = x1 + w1 * v1; } }
;                 af[ks] = __builtin_bit_cast(bf16x8, pg8::pack8(x0, x1)); }
.LBB0_616:
	ds_read_b128 v[8:11], v186 offset:8832
	ds_read_b128 v[12:15], v186 offset:8848
	s_waitcnt vmcnt(11)
	v_lshlrev_b32_e32 v16, 16, v110
	v_and_b32_e32 v17, 0xffff0000, v110
	v_lshlrev_b32_e32 v18, 16, v111
	v_and_b32_e32 v19, 0xffff0000, v111
	v_lshlrev_b32_e32 v20, 16, v108
	v_and_b32_e32 v21, 0xffff0000, v108
	v_lshlrev_b32_e32 v22, 16, v109
	v_and_b32_e32 v23, 0xffff0000, v109
	s_waitcnt lgkmcnt(1)
	v_pk_fma_f32 v[2:3], v[10:11], v[22:23], v[2:3]
	v_pk_fma_f32 v[0:1], v[8:9], v[20:21], v[0:1]
	s_waitcnt lgkmcnt(0)
	v_pk_fma_f32 v[6:7], v[14:15], v[18:19], v[6:7]
	v_pk_fma_f32 v[4:5], v[12:13], v[16:17], v[4:5]
.LBB0_617:
	s_or_b64 exec, exec, s[10:11]
	ds_read_b128 v[8:11], v186 offset:9088
	ds_read_b128 v[12:15], v186 offset:9104
	s_waitcnt vmcnt(9)
	v_lshlrev_b32_e32 v16, 16, v118
	v_and_b32_e32 v17, 0xffff0000, v118
	v_lshlrev_b32_e32 v18, 16, v119
	v_and_b32_e32 v19, 0xffff0000, v119
	s_waitcnt lgkmcnt(0)
	v_pk_fma_f32 v[6:7], v[14:15], v[18:19], v[6:7]
	v_pk_fma_f32 v[4:5], v[12:13], v[16:17], v[4:5]
	v_lshlrev_b32_e32 v12, 16, v116
	v_and_b32_e32 v13, 0xffff0000, v116
	v_lshlrev_b32_e32 v14, 16, v117
	v_and_b32_e32 v15, 0xffff0000, v117
	v_pk_fma_f32 v[2:3], v[10:11], v[14:15], v[2:3]
	v_pk_fma_f32 v[0:1], v[8:9], v[12:13], v[0:1]
	s_nop 0
	v_cvt_pk_bf16_f32 v132, v0, v1
	v_cvt_pk_bf16_f32 v133, v2, v3
	v_cvt_pk_bf16_f32 v134, v4, v5
	v_cvt_pk_bf16_f32 v135, v6, v7
	ds_read_b128 v[0:3], v188 offset:9216
	ds_read_b128 v[4:7], v188 offset:9232
	s_and_saveexec_b64 s[10:11], vcc
	s_cbranch_execz .LBB0_629
	ds_read_b128 v[8:11], v188 offset:8192
	ds_read_b128 v[12:15], v188 offset:8208
	v_lshlrev_b32_e32 v16, 16, v98
	v_and_b32_e32 v17, 0xffff0000, v98
	v_lshlrev_b32_e32 v18, 16, v99
	v_and_b32_e32 v19, 0xffff0000, v99
	v_lshlrev_b32_e32 v20, 16, v96
	v_and_b32_e32 v21, 0xffff0000, v96
	v_lshlrev_b32_e32 v22, 16, v97
	v_and_b32_e32 v23, 0xffff0000, v97
	s_waitcnt lgkmcnt(1)
	v_pk_fma_f32 v[2:3], v[10:11], v[22:23], v[2:3]
	v_pk_fma_f32 v[0:1], v[8:9], v[20:21], v[0:1]
	s_waitcnt lgkmcnt(0)
	v_pk_fma_f32 v[6:7], v[14:15], v[18:19], v[6:7]
	v_pk_fma_f32 v[4:5], v[12:13], v[16:17], v[4:5]
	s_or_b64 exec, exec, s[10:11]
	s_and_saveexec_b64 s[10:11], s[4:5]
	s_cbranch_execnz .LBB0_630

; #define LAS __attribute__((address_space(3)))
; __device__ __forceinline__ u32x4 pack8(const f32x4 a, const f32x4 b) { u32x4 w; w.x = cvt_pk_bf16(a[0], a[1]); w.y = cvt_pk_bf16(a[2], a[3]); w.z = cvt_pk_bf16(b[0], b[1]); w.w = cvt_pk_bf16(b[2], b[3]); return w; }
; #define LRU_LOAD_RAW(st_) do { const int t_ = ck * TC + (st_) * 32 + r32; const size_t m_ = (size_t)b * SEQ + t_; _Pragma("unroll") for (int ks = 0; ks < 4; ++ks) _Pragma("unroll") for (int j = 0; j < 4; ++j) { \
;             const int back_ = 3 - j; const size_t mm_ = (t_ >= back_) ? m_ - back_ : m_; raw[ks][j] = *(const u32x4*)(U + mm_ * NIN + C_LX + ch0 + 16 * ks + 8 * hi); } } while (0)
; __device__ __forceinline__ void lru_scan(LAS unsigned char* lds, const bf16* U, bf16* HR, bf16* PQ, float* AGG, const bf16* Wt, const float* conv_w, const float* conv_b,
;                                          const float* b_rg, const float* b_ig, const float* lam, int G, int c, int wbase) {
;     ...
;             for (int ks = 0; ks < 4; ++ks) { const int cl = 16 * ks + 8 * hi; f32x4 x0 = *(const LAS f32x4*)(cw + 256 + cl), x1 = *(const LAS f32x4*)(cw + 256 + cl + 4);
; #pragma unroll
;                 for (int j = 0; j < 4; ++j) { const int back = 3 - j; const bool ok = t >= back;
;                     f32x4 v0, v1; pg8::unpack8(raw[ks][j], v0, v1);
;                     const f32x4 w0 = *(const LAS f32x4*)(cw + j * 64 + cl), w1 = *(const LAS f32x4*)(cw + j * 64 + cl + 4);
;                     if (ok) { x0 = x0 + w0 * v0; x1 = x1 + w1 * v1; } }
;                 af[ks] = __builtin_bit_cast(bf16x8, pg8::pack8(x0, x1)); }
;             if (st < 3) LRU_LOAD_RAW(st + 1);
.LBB0_621:
	s_or_b64 exec, exec, s[4:5]
	ds_read_b128 v[8:11], v188 offset:8960
	ds_read_b128 v[12:15], v188 offset:8976
	s_waitcnt vmcnt(8)
	v_lshlrev_b32_e32 v16, 16, v122
	v_and_b32_e32 v17, 0xffff0000, v122
	v_lshlrev_b32_e32 v18, 16, v123
	v_and_b32_e32 v19, 0xffff0000, v123
	s_waitcnt lgkmcnt(0)
	v_pk_fma_f32 v[6:7], v[14:15], v[18:19], v[6:7]
	v_pk_fma_f32 v[4:5], v[12:13], v[16:17], v[4:5]
	v_lshlrev_b32_e32 v12, 16, v120
	v_and_b32_e32 v13, 0xffff0000, v120
	v_lshlrev_b32_e32 v14, 16, v121
	v_and_b32_e32 v15, 0xffff0000, v121
	s_cmpk_eq_i32 s34, 0x60
	v_pk_fma_f32 v[2:3], v[10:11], v[14:15], v[2:3]
	v_pk_fma_f32 v[0:1], v[8:9], v[12:13], v[0:1]
	s_nop 0
	v_cvt_pk_bf16_f32 v136, v0, v1
	v_cvt_pk_bf16_f32 v137, v2, v3
	v_cvt_pk_bf16_f32 v138, v4, v5
	v_cvt_pk_bf16_f32 v139, v6, v7
	s_cbranch_scc1 .LBB0_604
	v_lshl_add_u64 v[0:1], s[8:9], 0, v[154:155]
	v_add_co_u32_e32 v2, vcc, 0x1f850000, v0
	s_nop 1
	v_addc_co_u32_e32 v3, vcc, 0, v1, vcc
	v_add_co_u32_e32 v4, vcc, 0x1f853000, v0
	s_nop 1
	v_addc_co_u32_e32 v5, vcc, 0, v1, vcc
	v_add_co_u32_e32 v6, vcc, 0x1f856000, v0
	s_nop 1
	v_addc_co_u32_e32 v7, vcc, 0, v1, vcc
	v_add_co_u32_e32 v0, vcc, 0x1f858000, v0
	s_nop 1
	v_addc_co_u32_e32 v1, vcc, 0, v1, vcc
	global_load_dwordx4 v[60:63], v[2:3], off offset:2048
	global_load_dwordx4 v[64:67], v[2:3], off offset:2080
	global_load_dwordx4 v[68:71], v[4:5], off offset:1024
	global_load_dwordx4 v[72:75], v[4:5], off offset:1056
	global_load_dwordx4 v[76:79], v[6:7], off
	global_load_dwordx4 v[80:83], v[6:7], off offset:32
	global_load_dwordx4 v[84:87], v[0:1], off offset:3072
	global_load_dwordx4 v[88:91], v[0:1], off offset:3104
	global_load_dwordx4 v[92:95], v[2:3], off offset:2112
	global_load_dwordx4 v[96:99], v[2:3], off offset:2144
	global_load_dwordx4 v[100:103], v[4:5], off offset:1088
	global_load_dwordx4 v[104:107], v[4:5], off offset:1120
	global_load_dwordx4 v[108:111], v[6:7], off offset:64
	global_load_dwordx4 v[112:115], v[6:7], off offset:96
	global_load_dwordx4 v[116:119], v[0:1], off offset:3136
	global_load_dwordx4 v[120:123], v[0:1], off offset:3168
	s_branch .LBB0_604

; #define LAS __attribute__((address_space(3)))
; __device__ __forceinline__ u32x4 pack8(const f32x4 a, const f32x4 b) { u32x4 w; w.x = cvt_pk_bf16(a[0], a[1]); w.y = cvt_pk_bf16(a[2], a[3]); w.z = cvt_pk_bf16(b[0], b[1]); w.w = cvt_pk_bf16(b[2], b[3]); return w; }
; __device__ __forceinline__ void lru_scan(LAS unsigned char* lds, const bf16* U, bf16* HR, bf16* PQ, float* AGG, const bf16* Wt, const float* conv_w, const float* conv_b,
;                                          const float* b_rg, const float* b_ig, const float* lam, int G, int c, int wbase) {
;     ...
;             for (int ks = 0; ks < 4; ++ks) { const int cl = 16 * ks + 8 * hi; f32x4 x0 = *(const LAS f32x4*)(cw + 256 + cl), x1 = *(const LAS f32x4*)(cw + 256 + cl + 4);
; #pragma unroll
;                 for (int j = 0; j < 4; ++j) { const int back = 3 - j; const bool ok = t >= back;
;                     f32x4 v0, v1; pg8::unpack8(raw[ks][j], v0, v1);
;                     const f32x4 w0 = *(const LAS f32x4*)(cw + j * 64 + cl), w1 = *(const LAS f32x4*)(cw + j * 64 + cl + 4);
;                     if (ok) { x0 = x0 + w0 * v0; x1 = x1 + w1 * v1; } }
;                 af[ks] = __builtin_bit_cast(bf16x8, pg8::pack8(x0, x1)); }
.LBB0_624:
	ds_read_b128 v[10:13], v186 offset:8448
	ds_read_b128 v[14:17], v186 offset:8464
	s_waitcnt vmcnt(21)
	v_lshlrev_b32_e32 v18, 16, v70
	v_and_b32_e32 v19, 0xffff0000, v70
	v_lshlrev_b32_e32 v20, 16, v71
	v_and_b32_e32 v21, 0xffff0000, v71
	v_lshlrev_b32_e32 v22, 16, v68
	v_and_b32_e32 v23, 0xffff0000, v68
	v_lshlrev_b32_e32 v24, 16, v69
	v_and_b32_e32 v25, 0xffff0000, v69
	s_waitcnt lgkmcnt(1)
	v_pk_fma_f32 v[2:3], v[12:13], v[24:25], v[2:3]
	v_pk_fma_f32 v[0:1], v[10:11], v[22:23], v[0:1]
	s_waitcnt lgkmcnt(0)
	v_pk_fma_f32 v[6:7], v[16:17], v[20:21], v[6:7]
	v_pk_fma_f32 v[4:5], v[14:15], v[18:19], v[4:5]
	s_or_b64 exec, exec, s[6:7]
	v_cmp_ne_u32_e64 s[6:7], 0, v8
	s_and_saveexec_b64 s[10:11], s[6:7]
	s_cbranch_execnz .LBB0_608
	s_branch .LBB0_609

; #define LAS __attribute__((address_space(3)))
; __device__ __forceinline__ u32x4 pack8(const f32x4 a, const f32x4 b) { u32x4 w; w.x = cvt_pk_bf16(a[0], a[1]); w.y = cvt_pk_bf16(a[2], a[3]); w.z = cvt_pk_bf16(b[0], b[1]); w.w = cvt_pk_bf16(b[2], b[3]); return w; }
; __device__ __forceinline__ void lru_scan(LAS unsigned char* lds, const bf16* U, bf16* HR, bf16* PQ, float* AGG, const bf16* Wt, const float* conv_w, const float* conv_b,
;                                          const float* b_rg, const float* b_ig, const float* lam, int G, int c, int wbase) {
;     ...
;             for (int ks = 0; ks < 4; ++ks) { const int cl = 16 * ks + 8 * hi; f32x4 x0 = *(const LAS f32x4*)(cw + 256 + cl), x1 = *(const LAS f32x4*)(cw + 256 + cl + 4);
; #pragma unroll
;                 for (int j = 0; j < 4; ++j) { const int back = 3 - j; const bool ok = t >= back;
;                     f32x4 v0, v1; pg8::unpack8(raw[ks][j], v0, v1);
;                     const f32x4 w0 = *(const LAS f32x4*)(cw + j * 64 + cl), w1 = *(const LAS f32x4*)(cw + j * 64 + cl + 4);
;                     if (ok) { x0 = x0 + w0 * v0; x1 = x1 + w1 * v1; } }
;                 af[ks] = __builtin_bit_cast(bf16x8, pg8::pack8(x0, x1)); }
.LBB0_628:
	ds_read_b128 v[8:11], v186 offset:8576
	ds_read_b128 v[12:15], v186 offset:8592
	s_waitcnt vmcnt(13)
	v_lshlrev_b32_e32 v16, 16, v102
	v_and_b32_e32 v17, 0xffff0000, v102
	v_lshlrev_b32_e32 v18, 16, v103
	v_and_b32_e32 v19, 0xffff0000, v103
	v_lshlrev_b32_e32 v20, 16, v100
	v_and_b32_e32 v21, 0xffff0000, v100
	v_lshlrev_b32_e32 v22, 16, v101
	v_and_b32_e32 v23, 0xffff0000, v101
	s_waitcnt lgkmcnt(1)
	v_pk_fma_f32 v[2:3], v[10:11], v[22:23], v[2:3]
	v_pk_fma_f32 v[0:1], v[8:9], v[20:21], v[0:1]
	s_waitcnt lgkmcnt(0)
	v_pk_fma_f32 v[6:7], v[14:15], v[18:19], v[6:7]
	v_pk_fma_f32 v[4:5], v[12:13], v[16:17], v[4:5]
	s_or_b64 exec, exec, s[10:11]
	s_and_saveexec_b64 s[10:11], s[6:7]
	s_cbranch_execnz .LBB0_616
	s_branch .LBB0_617

; #define PG8_STAGE(bufoff, rs_, soff_, voff) do { _Pragma("unroll") for (int _i = 0; _i < 2; ++_i) \
;         __builtin_amdgcn_raw_ptr_buffer_load_lds(rs_, (LAS void*)(lds + (bufoff) + ldsw + _i * 8192), 16, (int)(voff)[_i], (int)(soff_), 0, 0); } while (0)
; #define PG8_LDA(dst, b, h) do { _Pragma("unroll") for (int m = 0; m < 4; ++m) dst[m] = PG8_LD2(lds + PG8_SA(b, h) + aoff + m * 2048); } while (0)
; #define PG8_LDB(dst, b, h) do { _Pragma("unroll") for (int n = 0; n < 2; ++n) dst[n] = PG8_LD2(lds + PG8_SB(b, h) + boff + n * 2048); } while (0)
; #define PG8_WAIT_V(n) asm volatile("s_waitcnt vmcnt(" #n ")" ::: "memory")
; #define PG8_WAIT_L(n) asm volatile("s_waitcnt lgkmcnt(" #n ")" ::: "memory")
; #define PG8_BAR __builtin_amdgcn_s_barrier()
; #define PG8_SCHED __builtin_amdgcn_sched_barrier(0)
; template <class Epi, class Sched, bool ALIGN_EPI = false, bool SP2 = false, bool FP8 = false>
; __device__ __forceinline__ void gemm_phase(LAS unsigned char* lds, const Gemm g, const Sched& S, const Epi& E, int wbase) {
;     ...
;             const unsigned a2 = last ? nA : cA + (unsigned)(t + 2) * kstep, b2 = last ? nB : cB + (unsigned)(t + 2) * kstep; const rsrc_t rA2 = (Sched::TWO && last) ? rAn : rAc, rB2 = (Sched::TWO && last) ? rBn : rBc;
;             const unsigned a3 = a2 + kstep, b3 = b2 + kstep;
;             if (last && has_next) S.a_ready(nxt);
;             if constexpr (SP2) {
;             PG8_LDB(B0, 0, 0); PG8_LDB(B1, 0, 1); PG8_SCHED; PG8_LDA(At, 0, 0); PG8_STAGE(PG8_SA(1, 1), rAc, a1 + hstep, voffA);
;             PG8_WAIT_V(8); PG8_WAIT_L(0); PG8_BAR; PG8_MMA(0, 0, At, B0); PG8_MMA(0, 1, At, B1); PG8_BAR; PG8_SCHED;
;             PG8_LDA(At, 0, 1); PG8_STAGE(PG8_SB(0, 0), rB2, b2, voffB); PG8_STAGE(PG8_SB(0, 1), rB2, b2 + hstep, voffB); PG8_STAGE(PG8_SA(0, 0), rA2, a2, voffA);
;             PG8_WAIT_V(8); PG8_WAIT_L(0); PG8_BAR; PG8_MMA(1, 0, At, B0); PG8_MMA(1, 1, At, B1); PG8_BAR; PG8_SCHED;
.LBB0_1348:
	v_add_u32_e32 v12, 0x10000, v199
	v_add_u32_e32 v28, 0x14000, v199
	ds_read_b128 v[0:3], v12
	ds_read_b128 v[4:7], v12 offset:1024
	ds_read_b128 v[8:11], v12 offset:2048
	ds_read_b128 v[12:15], v12 offset:3072
	ds_read_b128 v[16:19], v28
	ds_read_b128 v[20:23], v28 offset:1024
	ds_read_b128 v[24:27], v28 offset:2048
	ds_read_b128 v[28:31], v28 offset:3072
	s_add_i32 s6, s67, 0x80
	s_cmp_eq_u32 s65, s85
	s_cselect_b32 s54, s66, s6
	s_cselect_b64 vcc, -1, 0
	v_cndmask_b32_e32 v211, v210, v201, vcc
	s_or_b32 s78, s54, 0x80
	s_add_i32 s6, s41, s67
	s_mov_b32 m0, s76
	ds_read_b128 v[32:35], v200
	ds_read_b128 v[36:39], v200 offset:1024
	ds_read_b128 v[40:43], v200 offset:2048
	ds_read_b128 v[44:47], v200 offset:3072
	ds_read_b128 v[48:51], v200 offset:4096
	ds_read_b128 v[52:55], v200 offset:5120
	ds_read_b128 v[56:59], v200 offset:6144
	ds_read_b128 v[60:63], v200 offset:7168
	v_readfirstlane_b32 s55, v211
	s_add_i32 s20, s55, s41
	buffer_load_dwordx4 v192, s[36:39], s6 offen lds
	s_mov_b32 m0, s77
	s_nop 0
	buffer_load_dwordx4 v195, s[36:39], s6 offen lds
	s_waitcnt vmcnt(8)
	s_waitcnt lgkmcnt(0)
	s_barrier
	s_setprio 1
	s_waitcnt lgkmcnt(6)
	v_mfma_scale_f32_16x16x128_f8f6f4 v[184:187], v[0:7], v[32:39], v[184:187], v224, v224 op_sel_hi:[0,0,0]
	v_mfma_scale_f32_16x16x128_f8f6f4 v[188:191], v[8:15], v[32:39], v[188:191], v224, v224 op_sel_hi:[0,0,0]
	s_waitcnt lgkmcnt(4)
	v_mfma_scale_f32_16x16x128_f8f6f4 v[168:171], v[0:7], v[40:47], v[168:171], v224, v224 op_sel_hi:[0,0,0]
	v_mfma_scale_f32_16x16x128_f8f6f4 v[172:175], v[8:15], v[40:47], v[172:175], v224, v224 op_sel_hi:[0,0,0]
	s_waitcnt lgkmcnt(2)
	v_mfma_scale_f32_16x16x128_f8f6f4 v[152:155], v[0:7], v[48:55], v[152:155], v224, v224 op_sel_hi:[0,0,0]
	v_mfma_scale_f32_16x16x128_f8f6f4 v[156:159], v[8:15], v[48:55], v[156:159], v224, v224 op_sel_hi:[0,0,0]
	s_waitcnt lgkmcnt(0)
	v_mfma_scale_f32_16x16x128_f8f6f4 v[136:139], v[0:7], v[56:63], v[136:139], v224, v224 op_sel_hi:[0,0,0]
	v_mfma_scale_f32_16x16x128_f8f6f4 v[140:143], v[8:15], v[56:63], v[140:143], v224, v224 op_sel_hi:[0,0,0]
	s_setprio 0
	s_setprio 1
	v_mfma_scale_f32_16x16x128_f8f6f4 v[176:179], v[16:23], v[32:39], v[176:179], v224, v224 op_sel_hi:[0,0,0]
	v_mfma_scale_f32_16x16x128_f8f6f4 v[180:183], v[24:31], v[32:39], v[180:183], v224, v224 op_sel_hi:[0,0,0]
	v_mfma_scale_f32_16x16x128_f8f6f4 v[160:163], v[16:23], v[40:47], v[160:163], v224, v224 op_sel_hi:[0,0,0]
	v_mfma_scale_f32_16x16x128_f8f6f4 v[164:167], v[24:31], v[40:47], v[164:167], v224, v224 op_sel_hi:[0,0,0]
	v_mfma_scale_f32_16x16x128_f8f6f4 v[144:147], v[16:23], v[48:55], v[144:147], v224, v224 op_sel_hi:[0,0,0]
	v_mfma_scale_f32_16x16x128_f8f6f4 v[148:151], v[24:31], v[48:55], v[148:151], v224, v224 op_sel_hi:[0,0,0]
	v_mfma_scale_f32_16x16x128_f8f6f4 v[128:131], v[16:23], v[56:63], v[128:131], v224, v224 op_sel_hi:[0,0,0]
	v_mfma_scale_f32_16x16x128_f8f6f4 v[132:135], v[24:31], v[56:63], v[132:135], v224, v224 op_sel_hi:[0,0,0]
	s_setprio 0
	s_barrier
	ds_read_b128 v[32:35], v200 offset:16384
	ds_read_b128 v[36:39], v200 offset:17408
	ds_read_b128 v[40:43], v200 offset:18432
	ds_read_b128 v[44:47], v200 offset:19456
	ds_read_b128 v[48:51], v200 offset:20480
	ds_read_b128 v[52:55], v200 offset:21504
	ds_read_b128 v[56:59], v200 offset:22528
	ds_read_b128 v[60:63], v200 offset:23552
	s_mov_b32 s6, s38
	s_mov_b32 s7, s39
	s_mov_b32 m0, s43
	s_nop 0
	buffer_load_dwordx4 v194, s[4:7], s55 offen lds
	s_mov_b32 m0, s44
	s_nop 0
	buffer_load_dwordx4 v196, s[4:7], s55 offen lds
	s_mov_b32 m0, s45
	s_nop 0
	buffer_load_dwordx4 v194, s[4:7], s20 offen lds
	s_mov_b32 m0, s46
	s_nop 0
	buffer_load_dwordx4 v196, s[4:7], s20 offen lds
	s_mov_b32 m0, s42
	s_nop 0
	buffer_load_dwordx4 v192, s[36:39], s54 offen lds
	s_mov_b32 m0, s47
	s_nop 0
	buffer_load_dwordx4 v195, s[36:39], s54 offen lds
	s_waitcnt vmcnt(8)
	s_waitcnt lgkmcnt(0)
	s_barrier
	s_setprio 1
	s_waitcnt lgkmcnt(6)
	v_mfma_scale_f32_16x16x128_f8f6f4 v[120:123], v[0:7], v[32:39], v[120:123], v224, v224 op_sel_hi:[0,0,0]
	v_mfma_scale_f32_16x16x128_f8f6f4 v[124:127], v[8:15], v[32:39], v[124:127], v224, v224 op_sel_hi:[0,0,0]
	s_waitcnt lgkmcnt(4)
	v_mfma_scale_f32_16x16x128_f8f6f4 v[104:107], v[0:7], v[40:47], v[104:107], v224, v224 op_sel_hi:[0,0,0]
	v_mfma_scale_f32_16x16x128_f8f6f4 v[108:111], v[8:15], v[40:47], v[108:111], v224, v224 op_sel_hi:[0,0,0]
	s_waitcnt lgkmcnt(2)
	v_mfma_scale_f32_16x16x128_f8f6f4 v[88:91], v[0:7], v[48:55], v[88:91], v224, v224 op_sel_hi:[0,0,0]
	v_mfma_scale_f32_16x16x128_f8f6f4 v[92:95], v[8:15], v[48:55], v[92:95], v224, v224 op_sel_hi:[0,0,0]
	s_waitcnt lgkmcnt(0)
	v_mfma_scale_f32_16x16x128_f8f6f4 v[72:75], v[0:7], v[56:63], v[72:75], v224, v224 op_sel_hi:[0,0,0]
	v_mfma_scale_f32_16x16x128_f8f6f4 v[76:79], v[8:15], v[56:63], v[76:79], v224, v224 op_sel_hi:[0,0,0]
	s_setprio 0
	s_setprio 1
	v_mfma_scale_f32_16x16x128_f8f6f4 v[112:115], v[16:23], v[32:39], v[112:115], v224, v224 op_sel_hi:[0,0,0]
	v_mfma_scale_f32_16x16x128_f8f6f4 v[116:119], v[24:31], v[32:39], v[116:119], v224, v224 op_sel_hi:[0,0,0]
	v_mfma_scale_f32_16x16x128_f8f6f4 v[96:99], v[16:23], v[40:47], v[96:99], v224, v224 op_sel_hi:[0,0,0]
	v_mfma_scale_f32_16x16x128_f8f6f4 v[100:103], v[24:31], v[40:47], v[100:103], v224, v224 op_sel_hi:[0,0,0]
	v_mfma_scale_f32_16x16x128_f8f6f4 v[80:83], v[16:23], v[48:55], v[80:83], v224, v224 op_sel_hi:[0,0,0]
	v_mfma_scale_f32_16x16x128_f8f6f4 v[84:87], v[24:31], v[48:55], v[84:87], v224, v224 op_sel_hi:[0,0,0]
	v_mfma_scale_f32_16x16x128_f8f6f4 v[68:71], v[16:23], v[56:63], v[68:71], v224, v224 op_sel_hi:[0,0,0]
	v_mfma_scale_f32_16x16x128_f8f6f4 v[64:67], v[24:31], v[56:63], v[64:67], v224, v224 op_sel_hi:[0,0,0]
	s_setprio 0
	s_barrier
; #define PG8_STAGE(bufoff, rs_, soff_, voff) do { _Pragma("unroll") for (int _i = 0; _i < 2; ++_i) \
;         __builtin_amdgcn_raw_ptr_buffer_load_lds(rs_, (LAS void*)(lds + (bufoff) + ldsw + _i * 8192), 16, (int)(voff)[_i], (int)(soff_), 0, 0); } while (0)
; #define PG8_LDA(dst, b, h) do { _Pragma("unroll") for (int m = 0; m < 4; ++m) dst[m] = PG8_LD2(lds + PG8_SA(b, h) + aoff + m * 2048); } while (0)
; #define PG8_LDB(dst, b, h) do { _Pragma("unroll") for (int n = 0; n < 2; ++n) dst[n] = PG8_LD2(lds + PG8_SB(b, h) + boff + n * 2048); } while (0)
; #define PG8_WAIT_V(n) asm volatile("s_waitcnt vmcnt(" #n ")" ::: "memory")
; #define PG8_WAIT_L(n) asm volatile("s_waitcnt lgkmcnt(" #n ")" ::: "memory")
; #define PG8_BAR __builtin_amdgcn_s_barrier()
; #define PG8_SCHED __builtin_amdgcn_sched_barrier(0)
; template <class Epi, class Sched, bool ALIGN_EPI = false, bool SP2 = false, bool FP8 = false>
; __device__ __forceinline__ void gemm_phase(LAS unsigned char* lds, const Gemm g, const Sched& S, const Epi& E, int wbase) {
;     ...
;         for (int t = 0; t < nt; t += 2) {
;     ...
;             PG8_LDB(B0, 1, 0); PG8_LDB(B1, 1, 1); PG8_SCHED; PG8_LDA(At, 1, 0); PG8_STAGE(PG8_SA(0, 1), rA2, a2 + hstep, voffA);
;             PG8_WAIT_V(8); PG8_WAIT_L(0); PG8_BAR; PG8_MMA(0, 0, At, B0); PG8_MMA(0, 1, At, B1); PG8_BAR; PG8_SCHED;
;             PG8_LDA(At, 1, 1); PG8_STAGE(PG8_SB(1, 0), rB2, b3, voffB); PG8_STAGE(PG8_SB(1, 1), rB2, b3 + hstep, voffB); PG8_STAGE(PG8_SA(1, 0), rA2, a3, voffA);
;             PG8_WAIT_V(8); PG8_WAIT_L(0); PG8_BAR; PG8_MMA(1, 0, At, B0); PG8_MMA(1, 1, At, B1); PG8_BAR; PG8_SCHED;
	v_add_u32_e32 v12, 0x18000, v199
	v_add_u32_e32 v28, 0x1c000, v199
	ds_read_b128 v[0:3], v12
	ds_read_b128 v[4:7], v12 offset:1024
	ds_read_b128 v[8:11], v12 offset:2048
	ds_read_b128 v[12:15], v12 offset:3072
	ds_read_b128 v[16:19], v28
	ds_read_b128 v[20:23], v28 offset:1024
	ds_read_b128 v[24:27], v28 offset:2048
	ds_read_b128 v[28:31], v28 offset:3072
	s_add_i32 s54, s54, s41
	s_mov_b32 m0, s48
	ds_read_b128 v[32:35], v200 offset:32768
	ds_read_b128 v[36:39], v200 offset:33792
	ds_read_b128 v[40:43], v200 offset:34816
	ds_read_b128 v[44:47], v200 offset:35840
	ds_read_b128 v[48:51], v200 offset:36864
	ds_read_b128 v[52:55], v200 offset:37888
	ds_read_b128 v[56:59], v200 offset:38912
	ds_read_b128 v[60:63], v200 offset:39936
	buffer_load_dwordx4 v192, s[36:39], s54 offen lds
	s_mov_b32 m0, s52
	s_nop 0
	buffer_load_dwordx4 v195, s[36:39], s54 offen lds
	s_waitcnt vmcnt(8)
	s_waitcnt lgkmcnt(0)
	s_barrier
	s_setprio 1
	s_waitcnt lgkmcnt(6)
	v_mfma_scale_f32_16x16x128_f8f6f4 v[184:187], v[0:7], v[32:39], v[184:187], v224, v224 op_sel_hi:[0,0,0]
	v_mfma_scale_f32_16x16x128_f8f6f4 v[188:191], v[8:15], v[32:39], v[188:191], v224, v224 op_sel_hi:[0,0,0]
	s_waitcnt lgkmcnt(4)
	v_mfma_scale_f32_16x16x128_f8f6f4 v[168:171], v[0:7], v[40:47], v[168:171], v224, v224 op_sel_hi:[0,0,0]
	v_mfma_scale_f32_16x16x128_f8f6f4 v[172:175], v[8:15], v[40:47], v[172:175], v224, v224 op_sel_hi:[0,0,0]
	s_waitcnt lgkmcnt(2)
	v_mfma_scale_f32_16x16x128_f8f6f4 v[152:155], v[0:7], v[48:55], v[152:155], v224, v224 op_sel_hi:[0,0,0]
	v_mfma_scale_f32_16x16x128_f8f6f4 v[156:159], v[8:15], v[48:55], v[156:159], v224, v224 op_sel_hi:[0,0,0]
	s_waitcnt lgkmcnt(0)
	v_mfma_scale_f32_16x16x128_f8f6f4 v[136:139], v[0:7], v[56:63], v[136:139], v224, v224 op_sel_hi:[0,0,0]
	v_mfma_scale_f32_16x16x128_f8f6f4 v[140:143], v[8:15], v[56:63], v[140:143], v224, v224 op_sel_hi:[0,0,0]
	s_setprio 0
	s_setprio 1
	v_mfma_scale_f32_16x16x128_f8f6f4 v[176:179], v[16:23], v[32:39], v[176:179], v224, v224 op_sel_hi:[0,0,0]
	v_mfma_scale_f32_16x16x128_f8f6f4 v[180:183], v[24:31], v[32:39], v[180:183], v224, v224 op_sel_hi:[0,0,0]
	v_mfma_scale_f32_16x16x128_f8f6f4 v[160:163], v[16:23], v[40:47], v[160:163], v224, v224 op_sel_hi:[0,0,0]
	v_mfma_scale_f32_16x16x128_f8f6f4 v[164:167], v[24:31], v[40:47], v[164:167], v224, v224 op_sel_hi:[0,0,0]
	v_mfma_scale_f32_16x16x128_f8f6f4 v[144:147], v[16:23], v[48:55], v[144:147], v224, v224 op_sel_hi:[0,0,0]
	v_mfma_scale_f32_16x16x128_f8f6f4 v[148:151], v[24:31], v[48:55], v[148:151], v224, v224 op_sel_hi:[0,0,0]
	v_mfma_scale_f32_16x16x128_f8f6f4 v[128:131], v[16:23], v[56:63], v[128:131], v224, v224 op_sel_hi:[0,0,0]
	v_mfma_scale_f32_16x16x128_f8f6f4 v[132:135], v[24:31], v[56:63], v[132:135], v224, v224 op_sel_hi:[0,0,0]
	s_setprio 0
	s_barrier
	ds_read_b128 v[32:35], v200 offset:49152
	ds_read_b128 v[36:39], v200 offset:50176
	ds_read_b128 v[40:43], v200 offset:51200
	ds_read_b128 v[44:47], v200 offset:52224
	ds_read_b128 v[48:51], v200 offset:53248
	ds_read_b128 v[52:55], v200 offset:54272
	ds_read_b128 v[56:59], v200 offset:55296
	ds_read_b128 v[60:63], v200 offset:56320
	s_addk_i32 s55, 0x80
	s_addk_i32 s20, 0x80
	s_mov_b32 m0, s57
	s_nop 0
	buffer_load_dwordx4 v194, s[4:7], s55 offen lds
	s_mov_b32 m0, s58
	s_nop 0
	buffer_load_dwordx4 v196, s[4:7], s55 offen lds
	s_mov_b32 m0, s61
	s_nop 0
	buffer_load_dwordx4 v194, s[4:7], s20 offen lds
	s_mov_b32 m0, s62
	s_nop 0
	buffer_load_dwordx4 v196, s[4:7], s20 offen lds
	s_mov_b32 m0, s59
	s_nop 0
	buffer_load_dwordx4 v192, s[36:39], s78 offen lds
	s_mov_b32 m0, s60
	s_nop 0
	buffer_load_dwordx4 v195, s[36:39], s78 offen lds
	s_waitcnt vmcnt(8)
	s_waitcnt lgkmcnt(0)
	s_barrier
	s_setprio 1
	s_waitcnt lgkmcnt(6)
	v_mfma_scale_f32_16x16x128_f8f6f4 v[120:123], v[0:7], v[32:39], v[120:123], v224, v224 op_sel_hi:[0,0,0]
	v_mfma_scale_f32_16x16x128_f8f6f4 v[124:127], v[8:15], v[32:39], v[124:127], v224, v224 op_sel_hi:[0,0,0]
	s_waitcnt lgkmcnt(4)
	v_mfma_scale_f32_16x16x128_f8f6f4 v[104:107], v[0:7], v[40:47], v[104:107], v224, v224 op_sel_hi:[0,0,0]
	v_mfma_scale_f32_16x16x128_f8f6f4 v[108:111], v[8:15], v[40:47], v[108:111], v224, v224 op_sel_hi:[0,0,0]
	s_waitcnt lgkmcnt(2)
	v_mfma_scale_f32_16x16x128_f8f6f4 v[88:91], v[0:7], v[48:55], v[88:91], v224, v224 op_sel_hi:[0,0,0]
	v_mfma_scale_f32_16x16x128_f8f6f4 v[92:95], v[8:15], v[48:55], v[92:95], v224, v224 op_sel_hi:[0,0,0]
	s_waitcnt lgkmcnt(0)
	v_mfma_scale_f32_16x16x128_f8f6f4 v[72:75], v[0:7], v[56:63], v[72:75], v224, v224 op_sel_hi:[0,0,0]
	v_mfma_scale_f32_16x16x128_f8f6f4 v[76:79], v[8:15], v[56:63], v[76:79], v224, v224 op_sel_hi:[0,0,0]
	s_setprio 0
	s_setprio 1
	v_mfma_scale_f32_16x16x128_f8f6f4 v[112:115], v[16:23], v[32:39], v[112:115], v224, v224 op_sel_hi:[0,0,0]
	v_mfma_scale_f32_16x16x128_f8f6f4 v[116:119], v[24:31], v[32:39], v[116:119], v224, v224 op_sel_hi:[0,0,0]
	v_mfma_scale_f32_16x16x128_f8f6f4 v[96:99], v[16:23], v[40:47], v[96:99], v224, v224 op_sel_hi:[0,0,0]
	v_mfma_scale_f32_16x16x128_f8f6f4 v[100:103], v[24:31], v[40:47], v[100:103], v224, v224 op_sel_hi:[0,0,0]
	v_mfma_scale_f32_16x16x128_f8f6f4 v[80:83], v[16:23], v[48:55], v[80:83], v224, v224 op_sel_hi:[0,0,0]
	v_mfma_scale_f32_16x16x128_f8f6f4 v[84:87], v[24:31], v[48:55], v[84:87], v224, v224 op_sel_hi:[0,0,0]
	v_mfma_scale_f32_16x16x128_f8f6f4 v[68:71], v[16:23], v[56:63], v[68:71], v224, v224 op_sel_hi:[0,0,0]
	v_mfma_scale_f32_16x16x128_f8f6f4 v[64:67], v[24:31], v[56:63], v[64:67], v224, v224 op_sel_hi:[0,0,0]
	s_setprio 0
	s_barrier
	s_add_i32 s85, s85, 2
	s_addk_i32 s67, 0x100
	s_cmp_ge_i32 s85, s53
	v_add_u32_e32 v210, 0x100, v210
	s_cbranch_scc0 .LBB0_1348
	v_readlane_b32 s54, v255, 25
	v_readlane_b32 s55, v255, 26
	s_and_b64 vcc, exec, s[18:19]
	s_cbranch_vccnz .LBB0_1367
	s_branch .LBB0_1368
